# paired single f32 adds of the softmax row sums merged into packed adds in the four attention loops
# baseline (speedup 1.0000x reference)
; DI void attn_unit_d8(unsigned char* lds, const AttnArgs& a) {
;     ...
;     auto expsum = [&](f32x16& sc, f32x4& l) __attribute__((always_inline)) {
; #pragma unroll
;         for (int i = 0; i < 16; ++i) sc[i] = __builtin_amdgcn_exp2f(sc[i]);
; #pragma unroll
;         for (int i = 0; i < 4; ++i) l += (f32x4){sc[4 * i], sc[4 * i + 1], sc[4 * i + 2], sc[4 * i + 3]};
;     };
;     auto pack8 = [&](const f32x16& s0, const f32x16& s1) __attribute__((always_inline)) -> v8i { v8i p;
; #pragma unroll
;         for (int g = 0; g < 4; ++g) { p[g] = (int)pk4_fp8_div16(s0[4 * g], s0[4 * g + 1], s0[4 * g + 2], s0[4 * g + 3]); p[4 + g] = (int)pk4_fp8_div16(s1[4 * g], s1[4 * g + 1], s1[4 * g + 2], s1[4 * g + 3]); }
;         return p; };
;     auto pack4 = [&](const f32x16& sc, v8i& p, const int o) __attribute__((always_inline)) {
; #pragma unroll
;         for (int g = 0; g < 4; ++g) p[o + g] = (int)pk4_fp8_div16(sc[4 * g], sc[4 * g + 1], sc[4 * g + 2], sc[4 * g + 3]); };
;     auto qk = [&](const unsigned char* Kb, int hh, f32x16& sa, f32x16& sb) __attribute__((always_inline)) { const v8i kf = rd32(Kb + koff + hh * 32 * A8_PITCH);
;         sa = mfma8(kf, qfa, (f32x16){}); sb = mfma8(kf, qfb, (f32x16){}); };
;     gload(a.t0, kreg0, vreg0); gload(a.t0 + 1, kreg1, vreg1); lstore(0, kreg0, vreg0); lstore(1, kreg1, vreg1);
;     gload(a.t0 + 2, kreg0, vreg0); lstore(2, kreg0, vreg0);
;     __syncthreads();
;     asm volatile("" : "+v"(qfa), "+v"(qfb));
;     f32x16 s0a, s0b, s1a, s1b;
;     qk(lds, 0, s0a, s0b);
;     if (wid >= 4) __builtin_amdgcn_s_setprio(1);
;     int sb = 0;
;     const v8i zz8 = (v8i){0, 0, 0, 0, 0, 0, 0, 0};
;     v8i PaX = zz8, PbX = zz8, PaY = zz8, PbY = zz8, vX0 = zz8, vX1 = zz8, vY0 = zz8, vY1 = zz8;
;     auto tile = [&](const unsigned char* Kb, const unsigned char* Kn, v8i& Pa, v8i& Pb, v8i& v0, v8i& v1, const v8i& Qa, const v8i& Qb, const v8i& w0, const v8i& w1) __attribute__((always_inline)) {
;         qk(Kb, 1, s1a, s1b);
;         v0 = rd32(Kb + voff); v1 = rd32(Kb + voff + 32 * A8_PITCH);
;         o0[0] = mfma8(w0, Qa, o0[0]); o1[0] = mfma8(w0, Qb, o1[0]); o0[1] = mfma8(w1, Qa, o0[1]); o1[1] = mfma8(w1, Qb, o1[1]);
;         expsum(s0a, l0); expsum(s0b, l1); pack4(s0a, Pa, 0); pack4(s0b, Pb, 0);
;         qk(Kn, 0, s0a, s0b);
;         expsum(s1a, l0); expsum(s1b, l1); pack4(s1a, Pa, 4); pack4(s1b, Pb, 4);
; #pragma unroll
.LBB0_663:
	s_cmp_gt_i32 s16, 3
	s_cselect_b32 s17, -4, 1
	s_add_i32 s18, s17, s16
	s_mul_i32 s6, s16, 0x2800
	s_cmp_gt_i32 s16, 2
	v_mfma_f32_32x32x64_f8f6f4 v[50:65], v[154:161], v[138:145], v[50:65]
	v_exp_f32_e32 v192, v90
	v_add_u32_e32 v90, s6, v218
	s_cselect_b32 s6, -3, 2
	s_add_i32 s6, s6, s16
	s_cmp_gt_i32 s16, 1
	s_cselect_b32 s19, -2, 3
	s_add_i32 s19, s19, s16
	s_cmp_gt_i32 s16, 0
	s_cselect_b32 s49, -1, 4
	s_min_u32 s54, s46, 64
	s_add_i32 s49, s49, s16
	s_cmp_lt_u32 s46, 61
	s_mul_i32 s17, s6, 0x2800
	s_mov_b32 s16, s6
	s_cselect_b64 s[52:53], -1, 0
	s_lshl_b32 s6, s54, 6
	s_add_i32 s54, s6, 0xc0
	s_add_i32 s55, s6, 0xfffff0c0
	s_and_b64 s[52:53], s[52:53], exec
	v_lshl_add_u64 v[98:99], v[182:183], 0, s[6:7]
	s_cselect_b32 s6, s54, s55
	s_cselect_b32 s53, s21, s48
	s_cselect_b32 s52, s20, s47
	s_min_u32 s56, s46, 63
	v_exp_f32_e32 v198, v82
	v_exp_f32_e32 v199, v83
	v_exp_f32_e32 v196, v84
	v_exp_f32_e32 v197, v85
	v_exp_f32_e32 v200, v86
	v_exp_f32_e32 v201, v87
	v_exp_f32_e32 v194, v88
	v_exp_f32_e32 v195, v89
	ds_read_b128 v[82:85], v90 offset:2560
	ds_read_b128 v[86:89], v90 offset:2576
	global_load_dwordx2 v[202:203], v[98:99], off offset:192
	v_add_u32_e32 v98, s6, v215
	s_cmp_lt_u32 s46, 60
	v_ashrrev_i32_e32 v99, 31, v98
	s_cselect_b64 s[54:55], -1, 0
	s_lshl_b32 s6, s56, 6
	v_lshlrev_b64 v[98:99], 8, v[98:99]
	s_add_i32 s56, s6, 0x100
	s_add_i32 s57, s6, 0xfffff100
	v_lshl_add_u64 v[98:99], s[52:53], 0, v[98:99]
	s_and_b64 s[52:53], s[54:55], exec
	s_cselect_b32 s54, s56, s57
	v_lshl_add_u64 v[220:221], v[98:99], 0, v[178:179]
	v_add_u32_e32 v98, s54, v215
	v_ashrrev_i32_e32 v99, 31, v98
	s_cselect_b32 s53, s21, s48
	s_cselect_b32 s52, s20, s47
	v_lshlrev_b64 v[98:99], 8, v[98:99]
	v_lshl_add_u64 v[100:101], v[182:183], 0, s[6:7]
	v_lshl_add_u64 v[98:99], s[52:53], 0, v[98:99]
	global_load_dwordx2 v[204:205], v[100:101], off offset:256
	v_lshl_add_u64 v[222:223], v[98:99], 0, v[178:179]
	s_waitcnt lgkmcnt(0)
	v_mfma_f32_32x32x64_f8f6f4 v[98:113], v[82:89], v[114:121], 0
	v_exp_f32_e32 v193, v91
	v_exp_f32_e32 v224, v92
	v_exp_f32_e32 v225, v93
	v_exp_f32_e32 v226, v94
	v_exp_f32_e32 v227, v95
	v_exp_f32_e32 v228, v96
	v_exp_f32_e32 v229, v97
	ds_read_b128 v[170:173], v90 offset:5120
	ds_read_b128 v[174:177], v90 offset:5136
	ds_read_b128 v[162:165], v90 offset:7680
	ds_read_b128 v[166:169], v90 offset:7696
	v_pk_add_f32 v[90:91], v[186:187], v[198:199]
	v_pk_add_f32 v[92:93], v[184:185], v[196:197]
	v_pk_add_f32 v[90:91], v[200:201], v[90:91]
	v_pk_add_f32 v[92:93], v[194:195], v[92:93]
	v_pk_add_f32 v[90:91], v[192:193], v[90:91]
	v_pk_add_f32 v[92:93], v[224:225], v[92:93]
	v_exp_f32_e32 v66, v66
	v_exp_f32_e32 v67, v67
	v_exp_f32_e32 v68, v68
	v_exp_f32_e32 v69, v69
	v_exp_f32_e32 v70, v70
	v_exp_f32_e32 v71, v71
	v_exp_f32_e32 v72, v72
	v_pk_add_f32 v[230:231], v[228:229], v[92:93]
	v_pk_add_f32 v[232:233], v[226:227], v[90:91]
	v_mfma_f32_32x32x64_f8f6f4 v[82:97], v[82:89], v[122:129], 0
	v_exp_f32_e32 v73, v73
	v_exp_f32_e32 v74, v74
	v_exp_f32_e32 v75, v75
	v_exp_f32_e32 v76, v76
	v_exp_f32_e32 v77, v77
	v_exp_f32_e32 v78, v78
	v_exp_f32_e32 v79, v79
	v_exp_f32_e32 v80, v80
	v_exp_f32_e32 v81, v81
	v_pk_add_f32 v[186:187], v[190:191], v[66:67]
	v_pk_add_f32 v[188:189], v[188:189], v[68:69]
	v_pk_add_f32 v[186:187], v[70:71], v[186:187]
	v_pk_add_f32 v[188:189], v[72:73], v[188:189]
	v_cvt_scalef32_pk_fp8_f32 v184, v198, v199, s36
	v_pk_add_f32 v[186:187], v[74:75], v[186:187]
	v_pk_add_f32 v[188:189], v[76:77], v[188:189]
	v_cvt_scalef32_pk_fp8_f32 v185, v200, v201, s36
	v_cvt_scalef32_pk_fp8_f32 v184, v196, v197, s36 op_sel:[0,0,0,1]
	v_pk_add_f32 v[190:191], v[78:79], v[186:187]
	v_pk_add_f32 v[188:189], v[80:81], v[188:189]
	v_mfma_f32_32x32x64_f8f6f4 v[2:17], v[154:161], v[130:137], v[2:17]
	s_mulk_i32 s18, 0x2800
	v_cvt_scalef32_pk_fp8_f32 v186, v192, v193, s36
	v_cvt_scalef32_pk_fp8_f32 v187, v226, v227, s36
	v_cvt_scalef32_pk_fp8_f32 v154, v66, v67, s36
	v_cvt_scalef32_pk_fp8_f32 v155, v70, v71, s36
	v_cvt_scalef32_pk_fp8_f32 v156, v74, v75, s36
	v_cvt_scalef32_pk_fp8_f32 v157, v78, v79, s36
	v_cvt_scalef32_pk_fp8_f32 v185, v194, v195, s36 op_sel:[0,0,0,1]
	v_add_u32_e32 v219, s18, v218
	v_cvt_scalef32_pk_fp8_f32 v186, v224, v225, s36 op_sel:[0,0,0,1]
	v_cvt_scalef32_pk_fp8_f32 v187, v228, v229, s36 op_sel:[0,0,0,1]
	v_cvt_scalef32_pk_fp8_f32 v154, v68, v69, s36 op_sel:[0,0,0,1]
	v_cvt_scalef32_pk_fp8_f32 v155, v72, v73, s36 op_sel:[0,0,0,1]
	v_cvt_scalef32_pk_fp8_f32 v156, v76, v77, s36 op_sel:[0,0,0,1]
	v_cvt_scalef32_pk_fp8_f32 v157, v80, v81, s36 op_sel:[0,0,0,1]
	v_exp_f32_e32 v98, v98
	v_exp_f32_e32 v99, v99
	v_mfma_f32_32x32x64_f8f6f4 v[34:49], v[146:153], v[138:145], v[34:49]
	v_exp_f32_e32 v100, v100
	v_exp_f32_e32 v101, v101
	v_exp_f32_e32 v102, v102
	v_exp_f32_e32 v103, v103
	v_exp_f32_e32 v104, v104
	v_exp_f32_e32 v105, v105
	v_exp_f32_e32 v106, v106
	v_exp_f32_e32 v107, v107
	v_exp_f32_e32 v108, v108
	v_exp_f32_e32 v109, v109
	v_exp_f32_e32 v110, v110
	v_exp_f32_e32 v111, v111
	v_exp_f32_e32 v112, v112
	v_exp_f32_e32 v113, v113
	ds_read_b128 v[192:195], v219
	ds_read_b128 v[196:199], v219 offset:16
	v_pk_add_f32 v[66:67], v[232:233], v[98:99]
	v_pk_add_f32 v[68:69], v[230:231], v[100:101]
	v_pk_add_f32 v[66:67], v[102:103], v[66:67]
	v_pk_add_f32 v[68:69], v[104:105], v[68:69]
	v_pk_add_f32 v[66:67], v[106:107], v[66:67]
	v_pk_add_f32 v[68:69], v[108:109], v[68:69]
	v_pk_add_f32 v[140:141], v[110:111], v[66:67]
	v_pk_add_f32 v[138:139], v[112:113], v[68:69]
	v_mfma_f32_32x32x64_f8f6f4 v[18:33], v[146:153], v[130:137], v[18:33]
	v_exp_f32_e32 v82, v82
	v_exp_f32_e32 v83, v83
	v_exp_f32_e32 v84, v84
	v_exp_f32_e32 v85, v85
	v_exp_f32_e32 v86, v86
	v_exp_f32_e32 v87, v87
	v_exp_f32_e32 v88, v88
	v_exp_f32_e32 v89, v89
	v_exp_f32_e32 v90, v90
	v_exp_f32_e32 v91, v91
	v_exp_f32_e32 v92, v92
	v_exp_f32_e32 v93, v93
	v_exp_f32_e32 v94, v94
	v_exp_f32_e32 v95, v95
	v_exp_f32_e32 v96, v96
	v_exp_f32_e32 v97, v97
	v_pk_add_f32 v[66:67], v[190:191], v[82:83]
	v_pk_add_f32 v[68:69], v[188:189], v[84:85]
	v_pk_add_f32 v[66:67], v[86:87], v[66:67]
	v_pk_add_f32 v[68:69], v[88:89], v[68:69]
	v_pk_add_f32 v[130:131], v[90:91], v[66:67]
	v_pk_add_f32 v[132:133], v[92:93], v[68:69]
	s_waitcnt lgkmcnt(0)
; DI void attn_unit_d8(unsigned char* lds, const AttnArgs& a) {
;     ...
;     auto expsum = [&](f32x16& sc, f32x4& l) __attribute__((always_inline)) {
; #pragma unroll
;         for (int i = 0; i < 16; ++i) sc[i] = __builtin_amdgcn_exp2f(sc[i]);
; #pragma unroll
;         for (int i = 0; i < 4; ++i) l += (f32x4){sc[4 * i], sc[4 * i + 1], sc[4 * i + 2], sc[4 * i + 3]};
;     };
;     auto pack8 = [&](const f32x16& s0, const f32x16& s1) __attribute__((always_inline)) -> v8i { v8i p;
; #pragma unroll
;         for (int g = 0; g < 4; ++g) { p[g] = (int)pk4_fp8_div16(s0[4 * g], s0[4 * g + 1], s0[4 * g + 2], s0[4 * g + 3]); p[4 + g] = (int)pk4_fp8_div16(s1[4 * g], s1[4 * g + 1], s1[4 * g + 2], s1[4 * g + 3]); }
;         return p; };
;     auto pack4 = [&](const f32x16& sc, v8i& p, const int o) __attribute__((always_inline)) {
; #pragma unroll
;         for (int g = 0; g < 4; ++g) p[o + g] = (int)pk4_fp8_div16(sc[4 * g], sc[4 * g + 1], sc[4 * g + 2], sc[4 * g + 3]); };
;     auto qk = [&](const unsigned char* Kb, int hh, f32x16& sa, f32x16& sb) __attribute__((always_inline)) { const v8i kf = rd32(Kb + koff + hh * 32 * A8_PITCH);
;         sa = mfma8(kf, qfa, (f32x16){}); sb = mfma8(kf, qfb, (f32x16){}); };
;     gload(a.t0, kreg0, vreg0); gload(a.t0 + 1, kreg1, vreg1); lstore(0, kreg0, vreg0); lstore(1, kreg1, vreg1);
;     gload(a.t0 + 2, kreg0, vreg0); lstore(2, kreg0, vreg0);
;     __syncthreads();
;     asm volatile("" : "+v"(qfa), "+v"(qfb));
;     f32x16 s0a, s0b, s1a, s1b;
;     qk(lds, 0, s0a, s0b);
;     if (wid >= 4) __builtin_amdgcn_s_setprio(1);
;     int sb = 0;
;     const v8i zz8 = (v8i){0, 0, 0, 0, 0, 0, 0, 0};
;     v8i PaX = zz8, PbX = zz8, PaY = zz8, PbY = zz8, vX0 = zz8, vX1 = zz8, vY0 = zz8, vY1 = zz8;
;     auto tile = [&](const unsigned char* Kb, const unsigned char* Kn, v8i& Pa, v8i& Pb, v8i& v0, v8i& v1, const v8i& Qa, const v8i& Qb, const v8i& w0, const v8i& w1) __attribute__((always_inline)) {
;         qk(Kb, 1, s1a, s1b);
;         v0 = rd32(Kb + voff); v1 = rd32(Kb + voff + 32 * A8_PITCH);
;         o0[0] = mfma8(w0, Qa, o0[0]); o1[0] = mfma8(w0, Qb, o1[0]); o0[1] = mfma8(w1, Qa, o0[1]); o1[1] = mfma8(w1, Qb, o1[1]);
;         expsum(s0a, l0); expsum(s0b, l1); pack4(s0a, Pa, 0); pack4(s0b, Pb, 0);
;         qk(Kn, 0, s0a, s0b);
;         expsum(s1a, l0); expsum(s1b, l1); pack4(s1a, Pa, 4); pack4(s1b, Pb, 4);
; #pragma unroll
	v_mfma_f32_32x32x64_f8f6f4 v[66:81], v[192:199], v[114:121], 0
	v_cvt_scalef32_pk_fp8_f32 v188, v98, v99, s36
	v_cvt_scalef32_pk_fp8_f32 v189, v102, v103, s36
	v_cvt_scalef32_pk_fp8_f32 v190, v106, v107, s36
	v_cvt_scalef32_pk_fp8_f32 v191, v110, v111, s36
	v_cvt_scalef32_pk_fp8_f32 v158, v82, v83, s36
	v_cvt_scalef32_pk_fp8_f32 v159, v86, v87, s36
	v_pk_add_f32 v[142:143], v[96:97], v[132:133]
	v_pk_add_f32 v[144:145], v[94:95], v[130:131]
	v_cvt_scalef32_pk_fp8_f32 v160, v90, v91, s36
	v_cvt_scalef32_pk_fp8_f32 v188, v100, v101, s36 op_sel:[0,0,0,1]
	v_cvt_scalef32_pk_fp8_f32 v189, v104, v105, s36 op_sel:[0,0,0,1]
	v_cvt_scalef32_pk_fp8_f32 v190, v108, v109, s36 op_sel:[0,0,0,1]
	v_cvt_scalef32_pk_fp8_f32 v191, v112, v113, s36 op_sel:[0,0,0,1]
	v_cvt_scalef32_pk_fp8_f32 v158, v84, v85, s36 op_sel:[0,0,0,1]
	v_cvt_scalef32_pk_fp8_f32 v159, v88, v89, s36 op_sel:[0,0,0,1]
	v_mfma_f32_32x32x64_f8f6f4 v[98:113], v[192:199], v[122:129], 0
	global_load_dwordx2 v[192:193], v[220:221], off
	global_load_dwordx2 v[194:195], v[222:223], off
	ds_read_b128 v[130:133], v219 offset:2560
	ds_read_b128 v[134:137], v219 offset:2576
	s_mulk_i32 s19, 0x2800
	v_exp_f32_e32 v146, v66
	s_add_i32 s80, s61, 0
	v_exp_f32_e32 v147, v67
	s_lshr_b32 s73, s80, 2
	v_exp_f32_e32 v148, v68
	s_lshl_b32 s73, s73, 9
	v_exp_f32_e32 v149, v69
	s_add_i32 s73, s73, s42
	s_add_i32 s19, s19, 0
	v_cvt_scalef32_pk_fp8_f32 v161, v94, v95, s36
	v_exp_f32_e32 v150, v70
	s_mul_i32 s75, s73, 0xaaab
	v_exp_f32_e32 v151, v71
	s_lshr_b32 s75, s75, 22
	v_exp_f32_e32 v152, v72
	s_mul_i32 s76, s75, 0x60
	v_exp_f32_e32 v153, v73
	s_sub_i32 s76, s73, s76
	v_add_u32_e32 v224, s19, v216
	v_add_u32_e32 v225, s19, v217
	v_cvt_scalef32_pk_fp8_f32 v160, v92, v93, s36 op_sel:[0,0,0,1]
	v_cvt_scalef32_pk_fp8_f32 v161, v96, v97, s36 op_sel:[0,0,0,1]
	v_exp_f32_e32 v196, v74
	s_lshr_b32 s77, s76, 6
	v_exp_f32_e32 v197, v75
	s_lshl_b32 s78, s77, 6
	v_exp_f32_e32 v198, v76
	s_sub_i32 s76, s76, s78
	v_exp_f32_e32 v199, v77
	s_sub_i32 s78, 3, s77
	v_exp_f32_e32 v200, v78
	s_lshr_b32 s79, s76, s78
	v_exp_f32_e32 v201, v79
	s_lshl_b32 s79, s79, 2
	v_exp_f32_e32 v220, v80
	s_and_b32 s81, s80, 3
	v_exp_f32_e32 v221, v81
	s_add_i32 s79, s79, s81
	s_waitcnt lgkmcnt(0)
; DI void attn_unit_d8(unsigned char* lds, const AttnArgs& a) {
;     ...
;     auto expsum = [&](f32x16& sc, f32x4& l) __attribute__((always_inline)) {
; #pragma unroll
;         for (int i = 0; i < 16; ++i) sc[i] = __builtin_amdgcn_exp2f(sc[i]);
; #pragma unroll
;         for (int i = 0; i < 4; ++i) l += (f32x4){sc[4 * i], sc[4 * i + 1], sc[4 * i + 2], sc[4 * i + 3]};
;     };
;     auto pack8 = [&](const f32x16& s0, const f32x16& s1) __attribute__((always_inline)) -> v8i { v8i p;
; #pragma unroll
;         for (int g = 0; g < 4; ++g) { p[g] = (int)pk4_fp8_div16(s0[4 * g], s0[4 * g + 1], s0[4 * g + 2], s0[4 * g + 3]); p[4 + g] = (int)pk4_fp8_div16(s1[4 * g], s1[4 * g + 1], s1[4 * g + 2], s1[4 * g + 3]); }
;         return p; };
;     auto pack4 = [&](const f32x16& sc, v8i& p, const int o) __attribute__((always_inline)) {
; #pragma unroll
;         for (int g = 0; g < 4; ++g) p[o + g] = (int)pk4_fp8_div16(sc[4 * g], sc[4 * g + 1], sc[4 * g + 2], sc[4 * g + 3]); };
;     auto qk = [&](const unsigned char* Kb, int hh, f32x16& sa, f32x16& sb) __attribute__((always_inline)) { const v8i kf = rd32(Kb + koff + hh * 32 * A8_PITCH);
;         sa = mfma8(kf, qfa, (f32x16){}); sb = mfma8(kf, qfb, (f32x16){}); };
;     gload(a.t0, kreg0, vreg0); gload(a.t0 + 1, kreg1, vreg1); lstore(0, kreg0, vreg0); lstore(1, kreg1, vreg1);
;     gload(a.t0 + 2, kreg0, vreg0); lstore(2, kreg0, vreg0);
;     __syncthreads();
;     asm volatile("" : "+v"(qfa), "+v"(qfb));
;     f32x16 s0a, s0b, s1a, s1b;
;     qk(lds, 0, s0a, s0b);
;     if (wid >= 4) __builtin_amdgcn_s_setprio(1);
;     int sb = 0;
;     const v8i zz8 = (v8i){0, 0, 0, 0, 0, 0, 0, 0};
;     v8i PaX = zz8, PbX = zz8, PaY = zz8, PbY = zz8, vX0 = zz8, vX1 = zz8, vY0 = zz8, vY1 = zz8;
;     auto tile = [&](const unsigned char* Kb, const unsigned char* Kn, v8i& Pa, v8i& Pb, v8i& v0, v8i& v1, const v8i& Qa, const v8i& Qb, const v8i& w0, const v8i& w1) __attribute__((always_inline)) {
;         qk(Kb, 1, s1a, s1b);
;         v0 = rd32(Kb + voff); v1 = rd32(Kb + voff + 32 * A8_PITCH);
;         o0[0] = mfma8(w0, Qa, o0[0]); o1[0] = mfma8(w0, Qb, o1[0]); o0[1] = mfma8(w1, Qa, o0[1]); o1[1] = mfma8(w1, Qb, o1[1]);
;         expsum(s0a, l0); expsum(s0b, l1); pack4(s0a, Pa, 0); pack4(s0b, Pb, 0);
;         qk(Kn, 0, s0a, s0b);
;         expsum(s1a, l0); expsum(s1b, l1); pack4(s1a, Pa, 4); pack4(s1b, Pb, 4);
; #pragma unroll
	v_mfma_f32_32x32x64_f8f6f4 v[82:97], v[130:137], v[114:121], 0
	v_pk_add_f32 v[66:67], v[140:141], v[146:147]
	v_pk_add_f32 v[68:69], v[138:139], v[148:149]
	v_pk_add_f32 v[66:67], v[150:151], v[66:67]
	v_pk_add_f32 v[68:69], v[152:153], v[68:69]
	v_pk_add_f32 v[138:139], v[196:197], v[66:67]
	v_pk_add_f32 v[140:141], v[198:199], v[68:69]
	v_exp_f32_e32 v98, v98
	s_lshl_b32 s79, s79, 5
	v_exp_f32_e32 v99, v99
	s_lshl_b32 s81, s63, 2
	v_exp_f32_e32 v100, v100
	s_add_i32 s81, s81, s79
	v_exp_f32_e32 v101, v101
	s_sub_i32 s78, 13, s77
	v_exp_f32_e32 v102, v102
	s_lshl_b32 s81, s81, s78
	v_exp_f32_e32 v103, v103
	s_lshr_b32 s78, 7, s77
	v_exp_f32_e32 v104, v104
	s_and_b32 s78, s76, s78
	v_exp_f32_e32 v105, v105
	s_lshl_b32 s72, s78, 10
	v_exp_f32_e32 v106, v106
	s_add_i32 s81, s81, s72
	v_exp_f32_e32 v107, v107
	s_add_i32 s72, s75, 0
	v_exp_f32_e32 v108, v108
	s_sub_i32 s80, 23, s77
	v_exp_f32_e32 v109, v109
	s_lshl_b32 s72, s72, s80
	v_exp_f32_e32 v110, v110
	s_add_i32 s81, s81, s72
	v_exp_f32_e32 v111, v111
	s_cmp_eq_u32 s77, 0
	s_cselect_b64 s[84:85], s[66:67], s[68:69]
	v_exp_f32_e32 v112, v112
	s_add_u32 s84, s84, s81
	s_addc_u32 s85, s85, 0
	v_exp_f32_e32 v113, v113
	s_lshr_b32 s80, 0x2000, s77
	v_mfma_f32_32x32x64_f8f6f4 v[66:81], v[130:137], v[122:129], 0
	v_pk_add_f32 v[130:131], v[144:145], v[98:99]
	v_pk_add_f32 v[132:133], v[142:143], v[100:101]
	v_pk_add_f32 v[142:143], v[102:103], v[130:131]
	v_pk_add_f32 v[132:133], v[104:105], v[132:133]
	v_pk_add_f32 v[134:135], v[220:221], v[140:141]
	v_pk_add_f32 v[136:137], v[200:201], v[138:139]
	v_pk_add_f32 v[142:143], v[106:107], v[142:143]
	v_pk_add_f32 v[132:133], v[108:109], v[132:133]
	v_cvt_scalef32_pk_fp8_f32 v138, v146, v147, s36
	v_cvt_scalef32_pk_fp8_f32 v139, v150, v151, s36
	v_cvt_scalef32_pk_fp8_f32 v140, v196, v197, s36
	v_cvt_scalef32_pk_fp8_f32 v141, v200, v201, s36
	v_cvt_scalef32_pk_fp8_f32 v130, v98, v99, s36
	v_cvt_scalef32_pk_fp8_f32 v131, v102, v103, s36
	v_pk_add_f32 v[146:147], v[112:113], v[132:133]
	v_pk_add_f32 v[150:151], v[110:111], v[142:143]
	v_mfma_f32_32x32x64_f8f6f4 v[50:65], v[170:177], v[184:191], v[50:65]
	v_exp_f32_e32 v82, v82
	s_and_b32 s72, s78, 3
	v_exp_f32_e32 v83, v83
	s_lshl_b32 s72, s72, 19
	v_exp_f32_e32 v84, v84
	s_lshr_b32 s81, s78, 2
	v_exp_f32_e32 v85, v85
	s_lshl_b32 s81, s81, 17
	v_add_u32_e32 v102, s17, v218
	v_exp_f32_e32 v86, v86
	s_add_i32 s72, s72, s81
	v_exp_f32_e32 v87, v87
	s_lshl_b32 s81, s78, 18
	v_exp_f32_e32 v88, v88
	s_cmp_eq_u32 s77, 0
	s_cselect_b32 s72, s72, s81
	v_exp_f32_e32 v89, v89
	s_mul_i32 s81, s77, 0x10000000
	v_cvt_scalef32_pk_fp8_f32 v130, v100, v101, s36 op_sel:[0,0,0,1]
	v_cvt_scalef32_pk_fp8_f32 v131, v104, v105, s36 op_sel:[0,0,0,1]
	v_exp_f32_e32 v90, v90
	s_add_i32 s81, s81, 0x1094000
	v_exp_f32_e32 v91, v91
	s_add_i32 s72, s72, s79
	v_exp_f32_e32 v92, v92
	s_sub_i32 s73, 21, s77
	v_exp_f32_e32 v93, v93
	s_lshl_b32 s73, s75, s73
	ds_read_b128 v[98:101], v102
	ds_read_b128 v[102:105], v102 offset:16
	v_cvt_scalef32_pk_fp8_f32 v138, v148, v149, s36 op_sel:[0,0,0,1]
	v_cvt_scalef32_pk_fp8_f32 v139, v152, v153, s36 op_sel:[0,0,0,1]
	v_cvt_scalef32_pk_fp8_f32 v140, v198, v199, s36 op_sel:[0,0,0,1]
	v_cvt_scalef32_pk_fp8_f32 v141, v220, v221, s36 op_sel:[0,0,0,1]
	v_exp_f32_e32 v94, v94
	s_add_i32 s72, s72, s73
	v_mfma_f32_32x32x64_f8f6f4 v[2:17], v[170:177], v[154:161], v[2:17]
	v_exp_f32_e32 v148, v96
	s_add_u32 s72, s72, s81
	v_cvt_scalef32_pk_fp8_f32 v132, v106, v107, s36
	v_exp_f32_e32 v149, v97
	s_or_b32 s79, s72, s77
	v_pk_add_f32 v[96:97], v[136:137], v[82:83]
	v_pk_add_f32 v[106:107], v[134:135], v[84:85]
	v_exp_f32_e32 v66, v66
	v_exp_f32_e32 v67, v67
	v_exp_f32_e32 v68, v68
	v_exp_f32_e32 v69, v69
	v_exp_f32_e32 v95, v95
	v_cvt_scalef32_pk_fp8_f32 v133, v110, v111, s36
	v_pk_add_f32 v[106:107], v[88:89], v[106:107]
	v_pk_add_f32 v[96:97], v[86:87], v[96:97]
	v_exp_f32_e32 v70, v70
	v_exp_f32_e32 v71, v71
	v_exp_f32_e32 v72, v72
	v_exp_f32_e32 v73, v73
	v_cvt_scalef32_pk_fp8_f32 v132, v108, v109, s36 op_sel:[0,0,0,1]
	v_cvt_scalef32_pk_fp8_f32 v133, v112, v113, s36 op_sel:[0,0,0,1]
	v_pk_add_f32 v[96:97], v[90:91], v[96:97]
	v_pk_add_f32 v[106:107], v[92:93], v[106:107]
	v_exp_f32_e32 v74, v74
	v_mfma_f32_32x32x64_f8f6f4 v[34:49], v[162:169], v[184:191], v[34:49]
	v_exp_f32_e32 v75, v75
	v_exp_f32_e32 v76, v76
	v_exp_f32_e32 v77, v77
	v_exp_f32_e32 v78, v78
	v_exp_f32_e32 v79, v79
	v_exp_f32_e32 v80, v80
	v_exp_f32_e32 v81, v81
	v_cvt_scalef32_pk_fp8_f32 v142, v82, v83, s36
	v_cvt_scalef32_pk_fp8_f32 v143, v86, v87, s36
	v_cvt_scalef32_pk_fp8_f32 v144, v90, v91, s36
	v_cvt_scalef32_pk_fp8_f32 v142, v84, v85, s36 op_sel:[0,0,0,1]
	v_pk_add_f32 v[82:83], v[150:151], v[66:67]
	v_pk_add_f32 v[84:85], v[146:147], v[68:69]
	s_mulk_i32 s49, 0x2800
	v_pk_add_f32 v[184:185], v[148:149], v[106:107]
	v_pk_add_f32 v[186:187], v[94:95], v[96:97]
	v_cvt_scalef32_pk_fp8_f32 v145, v94, v95, s36
	v_cvt_scalef32_pk_fp8_f32 v143, v88, v89, s36 op_sel:[0,0,0,1]
	v_cvt_scalef32_pk_fp8_f32 v144, v92, v93, s36 op_sel:[0,0,0,1]
	v_mfma_f32_32x32x64_f8f6f4 v[18:33], v[162:169], v[154:161], v[18:33]
	v_pk_add_f32 v[84:85], v[72:73], v[84:85]
	v_pk_add_f32 v[82:83], v[70:71], v[82:83]
	s_add_i32 s6, s49, 0
	v_pk_add_f32 v[82:83], v[74:75], v[82:83]
	v_pk_add_f32 v[84:85], v[76:77], v[84:85]
	v_cvt_scalef32_pk_fp8_f32 v134, v66, v67, s36
	v_cvt_scalef32_pk_fp8_f32 v135, v70, v71, s36
	v_cvt_scalef32_pk_fp8_f32 v136, v74, v75, s36
	v_cvt_scalef32_pk_fp8_f32 v137, v78, v79, s36
	v_pk_add_f32 v[188:189], v[80:81], v[84:85]
	v_pk_add_f32 v[190:191], v[78:79], v[82:83]
	v_add_u32_e32 v106, s6, v216
	v_add_u32_e32 v107, s6, v217
	v_cvt_scalef32_pk_fp8_f32 v145, v148, v149, s36 op_sel:[0,0,0,1]
	v_cvt_scalef32_pk_fp8_f32 v134, v68, v69, s36 op_sel:[0,0,0,1]
	v_cvt_scalef32_pk_fp8_f32 v135, v72, v73, s36 op_sel:[0,0,0,1]
	v_cvt_scalef32_pk_fp8_f32 v136, v76, v77, s36 op_sel:[0,0,0,1]
	v_cvt_scalef32_pk_fp8_f32 v137, v80, v81, s36 op_sel:[0,0,0,1]
	s_waitcnt lgkmcnt(0)
	v_mfma_f32_32x32x64_f8f6f4 v[82:97], v[98:105], v[114:121], 0
	ds_read_b128 v[154:157], v219 offset:5120
	ds_read_b128 v[158:161], v219 offset:5136
	ds_read_b128 v[146:149], v219 offset:7680
	ds_read_b128 v[150:153], v219 offset:7696
	s_cmpk_gt_i32 s42, 0x1ff
	s_cbranch_scc1 .Lmy_rd0_ldum
	s_add_i32 s72, s61, -1
	s_cmp_lt_u32 s72, 24
	s_cbranch_scc0 .Lmy_rd0_noc
	s_waitcnt vmcnt(4)
	v_cvt_scalef32_pk_fp8_f32 v236, v236, v240, s62
	v_cvt_scalef32_pk_fp8_f32 v237, v237, v241, s62
	v_cvt_scalef32_pk_fp8_f32 v238, v238, v242, s62
	v_cvt_scalef32_pk_fp8_f32 v239, v239, v243, s62
	v_cvt_scalef32_pk_fp8_f32 v236, v244, v248, s62 op_sel:[0,0,0,1]
	v_cvt_scalef32_pk_fp8_f32 v237, v245, v249, s62 op_sel:[0,0,0,1]
	v_cvt_scalef32_pk_fp8_f32 v238, v246, v250, s62 op_sel:[0,0,0,1]
	v_cvt_scalef32_pk_fp8_f32 v239, v247, v251, s62 op_sel:[0,0,0,1]
	ds_write_b32 v252, v236
	ds_write_b32 v252, v237 offset:36
	ds_write_b32 v252, v238 offset:72
	ds_write_b32 v252, v239 offset:108

; DI void attn_unit_a8(unsigned char* lds, const AttnArgs& a) {
;     ...
;     auto expsum = [&](f32x16& sc) __attribute__((always_inline)) {
; #pragma unroll
;         for (int i = 0; i < 16; ++i) sc[i] = __builtin_amdgcn_exp2f(sc[i]);
; #pragma unroll
;         for (int i = 0; i < 4; ++i) l0 += (f32x4){sc[4 * i], sc[4 * i + 1], sc[4 * i + 2], sc[4 * i + 3]};
;     };
;     auto pack8 = [&](const f32x16& s0, const f32x16& s1) __attribute__((always_inline)) -> v8i { v8i p;
; #pragma unroll
;         for (int g = 0; g < 4; ++g) { p[g] = (int)pk4_fp8_div16(s0[4 * g], s0[4 * g + 1], s0[4 * g + 2], s0[4 * g + 3]); p[4 + g] = (int)pk4_fp8_div16(s1[4 * g], s1[4 * g + 1], s1[4 * g + 2], s1[4 * g + 3]); }
;         return p; };
;     f32x4 wq[4];
;     const int wn4 = (tid & 63) * 4;
;     constexpr int WPITCH = 36;
;     auto w_decode = [&](int j, const float*& src, unsigned char*& dst, int& ld, int& n0, int& k0, bool& gu) __attribute__((always_inline)) {
;         const int g = (j >> 2) * 512 + a.wl, e = g / 96, rr = g - e * 96; KParamsPtr kp = kparams();
;         if (rr < 64) { src = kp->w_gu + ((size_t)a.wli * NE + e) * (1024 * 2048); dst = kp->ws + WS_WGU + (size_t)a.wli * SZ_WGU + (size_t)e * 2048 * 1024; ld = 2048; n0 = (rr & 7) * 256; k0 = ((rr >> 3) * 4 + (j & 3)) * 32; gu = true; }
;         else { const int q = rr - 64; src = kp->w_dn + ((size_t)a.wli * NE + e) * (1024 * 1024); dst = kp->ws + WS_WDN + (size_t)a.wli * SZ_WDN + (size_t)e * 1024 * 1024; ld = 1024; n0 = (q & 3) * 256; k0 = ((q >> 2) * 4 + (j & 3)) * 32; gu = false; } };
;     auto w_issue = [&](int j) __attribute__((always_inline)) { const float* src; unsigned char* dst; int ld, n0, k0; bool gu; w_decode(j, src, dst, ld, n0, k0, gu);
;         const float* p = src + (size_t)(k0 + 4 * wid) * ld + n0 + wn4;
;         wq[0] = __builtin_nontemporal_load((const f32x4*)p); wq[1] = __builtin_nontemporal_load((const f32x4*)(p + ld));
;         wq[2] = __builtin_nontemporal_load((const f32x4*)(p + (size_t)2 * ld)); wq[3] = __builtin_nontemporal_load((const f32x4*)(p + (size_t)3 * ld)); };
;     auto w_cvt = [&]() __attribute__((always_inline)) { unsigned char* t8 = lds + AT_WT + wn4 * WPITCH + 4 * wid;
; #pragma unroll
;         for (int j = 0; j < 4; ++j) *(unsigned*)(t8 + j * WPITCH) = pk4_fp8_mul64(wq[0][j], wq[1][j], wq[2][j], wq[3][j]); };
;     const int wcol = tid >> 1, whalf = tid & 1;
.LBB0_714:
	s_min_i32 s4, s56, 64
	s_add_i32 s6, s4, 3
	s_cmp_lt_u32 s56, 61
	s_cselect_b64 s[10:11], -1, 0
	s_lshl_b32 s4, s6, 6
	s_add_i32 s7, s4, 0xfffff000
	s_and_b64 s[12:13], s[10:11], exec
	s_cselect_b32 s4, s4, s7
	v_add_u32_e32 v42, s4, v154
	s_add_i32 s4, s8, 1
	s_cmp_lg_u32 s8, 2
	s_mov_b32 s9, s8
	s_cselect_b32 s8, s4, 0
	s_mul_i32 s4, s8, 0x4680
	v_add_u32_e32 v106, s4, v157
	ds_read_b128 v[34:37], v106
	ds_read_b128 v[38:41], v106 offset:16
	s_and_b64 s[10:11], s[10:11], exec
	v_ashrrev_i32_e32 v43, 31, v42
	s_cselect_b32 s10, s58, s60
	s_cselect_b32 s11, s59, s61
	s_ashr_i32 s7, s6, 31
	s_waitcnt lgkmcnt(0)
	v_mfma_f32_32x32x64_f8f6f4 v[50:65], v[34:41], v[98:105], 0
	v_lshlrev_b64 v[34:35], 7, v[42:43]
	s_lshl_b64 s[12:13], s[6:7], 6
	v_lshl_add_u64 v[34:35], s[10:11], 0, v[34:35]
	v_lshl_add_u64 v[34:35], v[34:35], 0, v[130:131]
	v_lshl_add_u64 v[42:43], v[132:133], 0, s[12:13]
	global_load_dwordx2 v[112:113], v[34:35], off
	ds_read_b128 v[34:37], v106 offset:2560
	ds_read_b128 v[38:41], v106 offset:2576
	global_load_dwordx2 v[114:115], v[42:43], off
	s_mulk_i32 s9, 0x4680
	v_add_u32_e32 v42, s9, v157
	v_exp_f32_e32 v82, v82
	v_exp_f32_e32 v83, v83
	v_exp_f32_e32 v86, v86
	v_exp_f32_e32 v87, v87
	v_exp_f32_e32 v90, v90
	v_exp_f32_e32 v91, v91
	v_exp_f32_e32 v94, v94
	v_exp_f32_e32 v95, v95
	v_exp_f32_e32 v124, v66
	v_exp_f32_e32 v125, v67
	v_exp_f32_e32 v146, v70
	v_exp_f32_e32 v147, v71
	v_exp_f32_e32 v74, v74
	v_exp_f32_e32 v75, v75
	v_exp_f32_e32 v78, v78
	v_exp_f32_e32 v79, v79
	ds_read_b128 v[116:119], v42 offset:5120
	ds_read_b128 v[120:123], v42 offset:5136
	ds_read_b128 v[138:141], v42 offset:7680
	ds_read_b128 v[142:145], v42 offset:7696
	v_exp_f32_e32 v84, v84
	v_exp_f32_e32 v85, v85
	v_exp_f32_e32 v88, v88
	v_exp_f32_e32 v89, v89
	v_exp_f32_e32 v92, v92
	v_exp_f32_e32 v93, v93
	v_exp_f32_e32 v96, v96
	v_exp_f32_e32 v97, v97
	v_exp_f32_e32 v126, v68
	v_exp_f32_e32 v127, v69
	v_exp_f32_e32 v148, v72
	v_exp_f32_e32 v149, v73
	v_exp_f32_e32 v76, v76
	v_exp_f32_e32 v77, v77
	v_exp_f32_e32 v80, v80
	v_exp_f32_e32 v81, v81
	v_cvt_scalef32_pk_fp8_f32 v66, v82, v83, s48
	v_cvt_scalef32_pk_fp8_f32 v70, v124, v125, s48
	v_cvt_scalef32_pk_fp8_f32 v67, v86, v87, s48
	v_cvt_scalef32_pk_fp8_f32 v71, v146, v147, s48
	v_cvt_scalef32_pk_fp8_f32 v68, v90, v91, s48
	v_cvt_scalef32_pk_fp8_f32 v72, v74, v75, s48
	v_cvt_scalef32_pk_fp8_f32 v69, v94, v95, s48
	v_cvt_scalef32_pk_fp8_f32 v73, v78, v79, s48
	v_cvt_scalef32_pk_fp8_f32 v66, v84, v85, s48 op_sel:[0,0,0,1]
	v_cvt_scalef32_pk_fp8_f32 v70, v126, v127, s48 op_sel:[0,0,0,1]
	v_cvt_scalef32_pk_fp8_f32 v67, v88, v89, s48 op_sel:[0,0,0,1]
	v_cvt_scalef32_pk_fp8_f32 v71, v148, v149, s48 op_sel:[0,0,0,1]
	v_cvt_scalef32_pk_fp8_f32 v68, v92, v93, s48 op_sel:[0,0,0,1]
	v_cvt_scalef32_pk_fp8_f32 v72, v76, v77, s48 op_sel:[0,0,0,1]
	v_cvt_scalef32_pk_fp8_f32 v69, v96, v97, s48 op_sel:[0,0,0,1]
	v_cvt_scalef32_pk_fp8_f32 v73, v80, v81, s48 op_sel:[0,0,0,1]
	s_waitcnt lgkmcnt(4)
	v_mfma_f32_32x32x64_f8f6f4 v[34:49], v[34:41], v[98:105], 0
	s_addk_i32 s4, 0x4680
	s_cmp_eq_u32 s8, 2
	v_pk_add_f32 v[110:111], v[110:111], v[84:85]
	v_pk_add_f32 v[82:83], v[108:109], v[82:83]
	s_cselect_b64 s[6:7], -1, 0
	v_pk_add_f32 v[84:85], v[88:89], v[110:111]
	v_pk_add_f32 v[82:83], v[86:87], v[82:83]
	v_pk_add_f32 v[84:85], v[92:93], v[84:85]
	v_pk_add_f32 v[82:83], v[90:91], v[82:83]
	s_and_b64 s[10:11], s[6:7], exec
	v_pk_add_f32 v[84:85], v[96:97], v[84:85]
	v_pk_add_f32 v[82:83], v[94:95], v[82:83]
	s_cselect_b32 s4, 0, s4
	v_pk_add_f32 v[82:83], v[124:125], v[82:83]
	v_pk_add_f32 v[84:85], v[126:127], v[84:85]
	s_waitcnt lgkmcnt(2)
	v_mfma_f32_32x32x64_f8f6f4 v[18:33], v[116:123], v[66:73], v[18:33]
	s_add_i32 s4, s4, 0
	v_pk_add_f32 v[84:85], v[148:149], v[84:85]
	v_pk_add_f32 v[82:83], v[146:147], v[82:83]
	v_pk_add_f32 v[76:77], v[76:77], v[84:85]
	v_pk_add_f32 v[74:75], v[74:75], v[82:83]
	v_pk_add_f32 v[110:111], v[80:81], v[76:77]
	v_pk_add_f32 v[108:109], v[78:79], v[74:75]
	s_cmpk_gt_u32 s56, 0x42
	s_waitcnt lgkmcnt(0)
	v_mfma_f32_32x32x64_f8f6f4 v[2:17], v[138:145], v[66:73], v[2:17]
	v_add_u32_e32 v66, s4, v155
	s_waitcnt vmcnt(3)
	ds_write_b64 v66, v[134:135]
	v_add_u32_e32 v66, s4, v156
	v_add_u32_e32 v66, 0x1400, v66
	s_waitcnt vmcnt(2)
	ds_write2_b32 v66, v136, v137 offset1:8
	s_waitcnt lgkmcnt(0)
	s_barrier
; DI void attn_unit_a8(unsigned char* lds, const AttnArgs& a) {
;     ...
;     auto expsum = [&](f32x16& sc) __attribute__((always_inline)) {
; #pragma unroll
;         for (int i = 0; i < 16; ++i) sc[i] = __builtin_amdgcn_exp2f(sc[i]);
; #pragma unroll
;         for (int i = 0; i < 4; ++i) l0 += (f32x4){sc[4 * i], sc[4 * i + 1], sc[4 * i + 2], sc[4 * i + 3]};
;     };
;     auto pack8 = [&](const f32x16& s0, const f32x16& s1) __attribute__((always_inline)) -> v8i { v8i p;
; #pragma unroll
;         for (int g = 0; g < 4; ++g) { p[g] = (int)pk4_fp8_div16(s0[4 * g], s0[4 * g + 1], s0[4 * g + 2], s0[4 * g + 3]); p[4 + g] = (int)pk4_fp8_div16(s1[4 * g], s1[4 * g + 1], s1[4 * g + 2], s1[4 * g + 3]); }
;         return p; };
;     f32x4 wq[4];
;     const int wn4 = (tid & 63) * 4;
;     constexpr int WPITCH = 36;
;     auto w_decode = [&](int j, const float*& src, unsigned char*& dst, int& ld, int& n0, int& k0, bool& gu) __attribute__((always_inline)) {
;         const int g = (j >> 2) * 512 + a.wl, e = g / 96, rr = g - e * 96; KParamsPtr kp = kparams();
;         if (rr < 64) { src = kp->w_gu + ((size_t)a.wli * NE + e) * (1024 * 2048); dst = kp->ws + WS_WGU + (size_t)a.wli * SZ_WGU + (size_t)e * 2048 * 1024; ld = 2048; n0 = (rr & 7) * 256; k0 = ((rr >> 3) * 4 + (j & 3)) * 32; gu = true; }
;         else { const int q = rr - 64; src = kp->w_dn + ((size_t)a.wli * NE + e) * (1024 * 1024); dst = kp->ws + WS_WDN + (size_t)a.wli * SZ_WDN + (size_t)e * 1024 * 1024; ld = 1024; n0 = (q & 3) * 256; k0 = ((q >> 2) * 4 + (j & 3)) * 32; gu = false; } };
;     auto w_issue = [&](int j) __attribute__((always_inline)) { const float* src; unsigned char* dst; int ld, n0, k0; bool gu; w_decode(j, src, dst, ld, n0, k0, gu);
;         const float* p = src + (size_t)(k0 + 4 * wid) * ld + n0 + wn4;
;         wq[0] = __builtin_nontemporal_load((const f32x4*)p); wq[1] = __builtin_nontemporal_load((const f32x4*)(p + ld));
;         wq[2] = __builtin_nontemporal_load((const f32x4*)(p + (size_t)2 * ld)); wq[3] = __builtin_nontemporal_load((const f32x4*)(p + (size_t)3 * ld)); };
;     auto w_cvt = [&]() __attribute__((always_inline)) { unsigned char* t8 = lds + AT_WT + wn4 * WPITCH + 4 * wid;
; #pragma unroll
;         for (int j = 0; j < 4; ++j) *(unsigned*)(t8 + j * WPITCH) = pk4_fp8_mul64(wq[0][j], wq[1][j], wq[2][j], wq[3][j]); };
;     const int wcol = tid >> 1, whalf = tid & 1;
	s_cbranch_scc1 .LBB0_716
	s_min_u32 s4, s56, 63
	s_cmp_lt_u32 s56, 60
	s_cselect_b64 s[10:11], -1, 0
	s_lshl_b32 s4, s4, 6
	s_add_i32 s9, s4, 0x100
	s_add_i32 s14, s4, 0xfffff100
	s_and_b64 s[12:13], s[10:11], exec
	s_cselect_b32 s9, s9, s14
	s_add_i32 s8, s8, 1
	s_and_b64 s[6:7], s[6:7], exec
	v_add_u32_e32 v82, s9, v154
	s_cselect_b32 s8, 0, s8
	s_and_b64 s[10:11], s[10:11], exec
	v_ashrrev_i32_e32 v83, 31, v82
	s_cselect_b32 s11, s59, s61
	s_cselect_b32 s10, s58, s60
	v_lshlrev_b64 v[82:83], 7, v[82:83]
	s_mul_i32 s6, s8, 0x4680
	v_lshl_add_u64 v[90:91], s[10:11], 0, v[82:83]
	v_add_u32_e32 v86, s6, v157
	v_lshl_add_u64 v[90:91], v[90:91], 0, v[130:131]
	ds_read_b128 v[66:69], v86 offset:2560
	ds_read_b128 v[70:73], v86 offset:2576
	ds_read_b128 v[82:85], v86
	ds_read_b128 v[86:89], v86 offset:16
	global_load_dwordx2 v[134:135], v[90:91], off
	v_lshl_add_u64 v[90:91], v[132:133], 0, s[4:5]
	global_load_dwordx2 v[136:137], v[90:91], off offset:256
	v_exp_f32_e32 v50, v50
	v_exp_f32_e32 v51, v51
	v_exp_f32_e32 v54, v54
	v_exp_f32_e32 v55, v55
	v_exp_f32_e32 v58, v58
	v_exp_f32_e32 v59, v59
	v_exp_f32_e32 v62, v62
	v_exp_f32_e32 v63, v63
	v_exp_f32_e32 v124, v34
	v_exp_f32_e32 v125, v35
	v_exp_f32_e32 v146, v38
	v_exp_f32_e32 v147, v39
	v_exp_f32_e32 v42, v42
	v_exp_f32_e32 v43, v43
	v_exp_f32_e32 v46, v46
	v_exp_f32_e32 v47, v47
	ds_read_b128 v[116:119], v106 offset:5120
	ds_read_b128 v[120:123], v106 offset:5136
	ds_read_b128 v[138:141], v106 offset:7680
	ds_read_b128 v[142:145], v106 offset:7696
	v_exp_f32_e32 v52, v52
	v_exp_f32_e32 v53, v53
	v_exp_f32_e32 v56, v56
	v_exp_f32_e32 v57, v57
	v_exp_f32_e32 v60, v60
	v_exp_f32_e32 v61, v61
	v_exp_f32_e32 v64, v64
	v_exp_f32_e32 v65, v65
	v_exp_f32_e32 v126, v36
	v_exp_f32_e32 v127, v37
	v_exp_f32_e32 v148, v40
	v_exp_f32_e32 v149, v41
	v_exp_f32_e32 v44, v44
	v_exp_f32_e32 v45, v45
	v_exp_f32_e32 v48, v48
	v_exp_f32_e32 v49, v49
	s_waitcnt lgkmcnt(6)
	v_mfma_f32_32x32x64_f8f6f4 v[66:81], v[66:73], v[98:105], 0
	v_cvt_scalef32_pk_fp8_f32 v34, v50, v51, s48
	v_cvt_scalef32_pk_fp8_f32 v38, v124, v125, s48
	v_cvt_scalef32_pk_fp8_f32 v35, v54, v55, s48
	v_cvt_scalef32_pk_fp8_f32 v39, v146, v147, s48
	v_cvt_scalef32_pk_fp8_f32 v36, v58, v59, s48
	v_cvt_scalef32_pk_fp8_f32 v40, v42, v43, s48
	v_cvt_scalef32_pk_fp8_f32 v37, v62, v63, s48
	v_cvt_scalef32_pk_fp8_f32 v41, v46, v47, s48
	v_cvt_scalef32_pk_fp8_f32 v34, v52, v53, s48 op_sel:[0,0,0,1]
	v_cvt_scalef32_pk_fp8_f32 v38, v126, v127, s48 op_sel:[0,0,0,1]
	v_cvt_scalef32_pk_fp8_f32 v35, v56, v57, s48 op_sel:[0,0,0,1]
	v_cvt_scalef32_pk_fp8_f32 v39, v148, v149, s48 op_sel:[0,0,0,1]
	v_cvt_scalef32_pk_fp8_f32 v36, v60, v61, s48 op_sel:[0,0,0,1]
	v_cvt_scalef32_pk_fp8_f32 v40, v44, v45, s48 op_sel:[0,0,0,1]
	v_cvt_scalef32_pk_fp8_f32 v37, v64, v65, s48 op_sel:[0,0,0,1]
	s_waitcnt lgkmcnt(4)
	v_mfma_f32_32x32x64_f8f6f4 v[82:97], v[82:89], v[98:105], 0
	v_cvt_scalef32_pk_fp8_f32 v41, v48, v49, s48 op_sel:[0,0,0,1]
	v_pk_add_f32 v[110:111], v[110:111], v[52:53]
	v_pk_add_f32 v[50:51], v[108:109], v[50:51]
	s_addk_i32 s6, 0x4680
	v_pk_add_f32 v[52:53], v[56:57], v[110:111]
	v_pk_add_f32 v[50:51], v[54:55], v[50:51]
	s_cmp_lg_u32 s8, 2
	v_pk_add_f32 v[50:51], v[58:59], v[50:51]
	v_pk_add_f32 v[52:53], v[60:61], v[52:53]
	s_cselect_b32 s4, s6, 0
	v_pk_add_f32 v[52:53], v[64:65], v[52:53]
	v_pk_add_f32 v[50:51], v[62:63], v[50:51]
	s_add_i32 s4, s4, 0
	v_pk_add_f32 v[50:51], v[124:125], v[50:51]
	v_pk_add_f32 v[52:53], v[126:127], v[52:53]
	s_waitcnt lgkmcnt(2)
	v_mfma_f32_32x32x64_f8f6f4 v[18:33], v[116:123], v[34:41], v[18:33]
	v_pk_add_f32 v[52:53], v[148:149], v[52:53]
	v_pk_add_f32 v[50:51], v[146:147], v[50:51]
	v_pk_add_f32 v[44:45], v[44:45], v[52:53]
	v_pk_add_f32 v[42:43], v[42:43], v[50:51]
	v_pk_add_f32 v[110:111], v[48:49], v[44:45]
	v_pk_add_f32 v[108:109], v[46:47], v[42:43]
	s_waitcnt lgkmcnt(0)
	v_mfma_f32_32x32x64_f8f6f4 v[2:17], v[138:145], v[34:41], v[2:17]
	v_add_u32_e32 v34, s4, v155
	s_waitcnt vmcnt(3)
	ds_write_b64 v34, v[112:113]
	v_add_u32_e32 v34, s4, v156
	v_add_u32_e32 v34, 0x1400, v34
	s_waitcnt vmcnt(2)
	ds_write2_b32 v34, v114, v115 offset1:8
	s_waitcnt lgkmcnt(0)
	s_barrier

; DI void attn_unit_d8(unsigned char* lds, const AttnArgs& a) {
;     ...
;     auto expsum = [&](f32x16& sc, f32x4& l) __attribute__((always_inline)) {
; #pragma unroll
;         for (int i = 0; i < 16; ++i) sc[i] = __builtin_amdgcn_exp2f(sc[i]);
; #pragma unroll
;         for (int i = 0; i < 4; ++i) l += (f32x4){sc[4 * i], sc[4 * i + 1], sc[4 * i + 2], sc[4 * i + 3]};
;     };
;     auto pack8 = [&](const f32x16& s0, const f32x16& s1) __attribute__((always_inline)) -> v8i { v8i p;
; #pragma unroll
;         for (int g = 0; g < 4; ++g) { p[g] = (int)pk4_fp8_div16(s0[4 * g], s0[4 * g + 1], s0[4 * g + 2], s0[4 * g + 3]); p[4 + g] = (int)pk4_fp8_div16(s1[4 * g], s1[4 * g + 1], s1[4 * g + 2], s1[4 * g + 3]); }
;         return p; };
;     auto pack4 = [&](const f32x16& sc, v8i& p, const int o) __attribute__((always_inline)) {
; #pragma unroll
;         for (int g = 0; g < 4; ++g) p[o + g] = (int)pk4_fp8_div16(sc[4 * g], sc[4 * g + 1], sc[4 * g + 2], sc[4 * g + 3]); };
;     auto qk = [&](const unsigned char* Kb, int hh, f32x16& sa, f32x16& sb) __attribute__((always_inline)) { const v8i kf = rd32(Kb + koff + hh * 32 * A8_PITCH);
;         sa = mfma8(kf, qfa, (f32x16){}); sb = mfma8(kf, qfb, (f32x16){}); };
;     gload(a.t0, kreg0, vreg0); gload(a.t0 + 1, kreg1, vreg1); lstore(0, kreg0, vreg0); lstore(1, kreg1, vreg1);
;     gload(a.t0 + 2, kreg0, vreg0); lstore(2, kreg0, vreg0);
;     __syncthreads();
;     asm volatile("" : "+v"(qfa), "+v"(qfb));
;     f32x16 s0a, s0b, s1a, s1b;
;     qk(lds, 0, s0a, s0b);
;     if (wid >= 4) __builtin_amdgcn_s_setprio(1);
;     int sb = 0;
;     const v8i zz8 = (v8i){0, 0, 0, 0, 0, 0, 0, 0};
;     v8i PaX = zz8, PbX = zz8, PaY = zz8, PbY = zz8, vX0 = zz8, vX1 = zz8, vY0 = zz8, vY1 = zz8;
;     auto tile = [&](const unsigned char* Kb, const unsigned char* Kn, v8i& Pa, v8i& Pb, v8i& v0, v8i& v1, const v8i& Qa, const v8i& Qb, const v8i& w0, const v8i& w1) __attribute__((always_inline)) {
;         qk(Kb, 1, s1a, s1b);
;         v0 = rd32(Kb + voff); v1 = rd32(Kb + voff + 32 * A8_PITCH);
;         o0[0] = mfma8(w0, Qa, o0[0]); o1[0] = mfma8(w0, Qb, o1[0]); o0[1] = mfma8(w1, Qa, o0[1]); o1[1] = mfma8(w1, Qb, o1[1]);
;         expsum(s0a, l0); expsum(s0b, l1); pack4(s0a, Pa, 0); pack4(s0b, Pb, 0);
;         qk(Kn, 0, s0a, s0b);
;         expsum(s1a, l0); expsum(s1b, l1); pack4(s1a, Pa, 4); pack4(s1b, Pb, 4);
; #pragma unroll
.LBB0_1888:
	s_add_i32 s22, s22, 2
	s_mul_i32 s8, s23, 0x2800
	s_cmp_gt_i32 s23, 3
	v_mfma_f32_32x32x64_f8f6f4 v[50:65], v[154:161], v[138:145], v[50:65]
	v_exp_f32_e32 v194, v90
	v_add_u32_e32 v90, s8, v219
	s_cselect_b32 s8, -4, 1
	s_add_i32 s51, s8, s23
	s_cmp_gt_i32 s23, 2
	s_cselect_b32 s8, -3, 2
	s_add_i32 s8, s8, s23
	s_cmp_gt_i32 s23, 1
	s_cselect_b32 s52, -2, 3
	s_add_i32 s52, s52, s23
	s_cmp_gt_i32 s23, 0
	s_cselect_b32 s53, -1, 4
	s_min_u32 s56, s22, 64
	s_add_i32 s53, s53, s23
	s_cmp_lt_u32 s22, 61
	s_mul_i32 s50, s8, 0x2800
	s_mov_b32 s23, s8
	s_cselect_b64 s[54:55], -1, 0
	s_lshl_b32 s8, s56, 6
	s_add_i32 s56, s8, 0xc0
	s_add_i32 s57, s8, 0xfffff0c0
	s_and_b64 s[54:55], s[54:55], exec
	v_lshl_add_u64 v[98:99], v[184:185], 0, s[8:9]
	s_cselect_b32 s8, s56, s57
	s_cselect_b32 s55, s19, s21
	s_cselect_b32 s54, s18, s20
	s_min_u32 s58, s22, 63
	v_exp_f32_e32 v200, v82
	v_exp_f32_e32 v201, v83
	v_exp_f32_e32 v198, v84
	v_exp_f32_e32 v199, v85
	v_exp_f32_e32 v202, v86
	v_exp_f32_e32 v203, v87
	v_exp_f32_e32 v196, v88
	v_exp_f32_e32 v197, v89
	ds_read_b128 v[82:85], v90 offset:2560
	ds_read_b128 v[86:89], v90 offset:2576
	global_load_dwordx2 v[204:205], v[98:99], off offset:192
	v_add_u32_e32 v98, s8, v182
	s_cmp_lt_u32 s22, 60
	v_ashrrev_i32_e32 v99, 31, v98
	s_cselect_b64 s[56:57], -1, 0
	s_lshl_b32 s8, s58, 6
	v_lshlrev_b64 v[98:99], 8, v[98:99]
	s_add_i32 s58, s8, 0x100
	s_add_i32 s59, s8, 0xfffff100
	v_lshl_add_u64 v[98:99], s[54:55], 0, v[98:99]
	s_and_b64 s[54:55], s[56:57], exec
	v_lshl_add_u64 v[100:101], v[184:185], 0, s[8:9]
	s_cselect_b32 s8, s58, s59
	v_lshl_add_u64 v[220:221], v[98:99], 0, v[178:179]
	v_add_u32_e32 v98, s8, v182
	v_ashrrev_i32_e32 v99, 31, v98
	s_cselect_b32 s55, s19, s21
	s_cselect_b32 s54, s18, s20
	v_lshlrev_b64 v[98:99], 8, v[98:99]
	v_lshl_add_u64 v[98:99], s[54:55], 0, v[98:99]
	global_load_dwordx2 v[206:207], v[100:101], off offset:256
	v_lshl_add_u64 v[222:223], v[98:99], 0, v[178:179]
	s_waitcnt lgkmcnt(0)
	v_mfma_f32_32x32x64_f8f6f4 v[98:113], v[82:89], v[114:121], 0
	v_exp_f32_e32 v195, v91
	v_exp_f32_e32 v224, v92
	v_exp_f32_e32 v225, v93
	v_exp_f32_e32 v226, v94
	v_exp_f32_e32 v227, v95
	v_exp_f32_e32 v228, v96
	v_exp_f32_e32 v229, v97
	ds_read_b128 v[170:173], v90 offset:5120
	ds_read_b128 v[174:177], v90 offset:5136
	ds_read_b128 v[162:165], v90 offset:7680
	ds_read_b128 v[166:169], v90 offset:7696
	v_pk_add_f32 v[90:91], v[188:189], v[200:201]
	v_pk_add_f32 v[92:93], v[186:187], v[198:199]
	v_pk_add_f32 v[90:91], v[202:203], v[90:91]
	v_pk_add_f32 v[92:93], v[196:197], v[92:93]
	v_pk_add_f32 v[90:91], v[194:195], v[90:91]
	v_pk_add_f32 v[92:93], v[224:225], v[92:93]
	v_exp_f32_e32 v66, v66
	v_exp_f32_e32 v67, v67
	v_exp_f32_e32 v68, v68
	v_exp_f32_e32 v69, v69
	v_exp_f32_e32 v70, v70
	v_exp_f32_e32 v71, v71
	v_exp_f32_e32 v72, v72
	v_pk_add_f32 v[230:231], v[228:229], v[92:93]
	v_pk_add_f32 v[232:233], v[226:227], v[90:91]
	v_mfma_f32_32x32x64_f8f6f4 v[82:97], v[82:89], v[122:129], 0
	v_exp_f32_e32 v73, v73
	v_exp_f32_e32 v74, v74
	v_exp_f32_e32 v75, v75
	v_exp_f32_e32 v76, v76
	v_exp_f32_e32 v77, v77
	v_exp_f32_e32 v78, v78
	v_exp_f32_e32 v79, v79
	v_exp_f32_e32 v80, v80
	v_exp_f32_e32 v81, v81
	v_pk_add_f32 v[188:189], v[192:193], v[66:67]
	v_pk_add_f32 v[190:191], v[190:191], v[68:69]
	v_pk_add_f32 v[188:189], v[70:71], v[188:189]
	v_pk_add_f32 v[190:191], v[72:73], v[190:191]
	v_cvt_scalef32_pk_fp8_f32 v186, v200, v201, s36
	v_pk_add_f32 v[188:189], v[74:75], v[188:189]
	v_pk_add_f32 v[190:191], v[76:77], v[190:191]
	v_cvt_scalef32_pk_fp8_f32 v187, v202, v203, s36
	v_cvt_scalef32_pk_fp8_f32 v186, v198, v199, s36 op_sel:[0,0,0,1]
	v_pk_add_f32 v[192:193], v[78:79], v[188:189]
	v_pk_add_f32 v[190:191], v[80:81], v[190:191]
	v_mfma_f32_32x32x64_f8f6f4 v[2:17], v[154:161], v[130:137], v[2:17]
	s_mulk_i32 s51, 0x2800
	v_cvt_scalef32_pk_fp8_f32 v188, v194, v195, s36
	v_cvt_scalef32_pk_fp8_f32 v189, v226, v227, s36
	v_cvt_scalef32_pk_fp8_f32 v154, v66, v67, s36
	v_cvt_scalef32_pk_fp8_f32 v155, v70, v71, s36
	v_cvt_scalef32_pk_fp8_f32 v156, v74, v75, s36
	v_cvt_scalef32_pk_fp8_f32 v157, v78, v79, s36
	v_cvt_scalef32_pk_fp8_f32 v187, v196, v197, s36 op_sel:[0,0,0,1]
	v_add_u32_e32 v234, s51, v219
	v_cvt_scalef32_pk_fp8_f32 v188, v224, v225, s36 op_sel:[0,0,0,1]
	v_cvt_scalef32_pk_fp8_f32 v189, v228, v229, s36 op_sel:[0,0,0,1]
	v_cvt_scalef32_pk_fp8_f32 v154, v68, v69, s36 op_sel:[0,0,0,1]
	v_cvt_scalef32_pk_fp8_f32 v155, v72, v73, s36 op_sel:[0,0,0,1]
	v_cvt_scalef32_pk_fp8_f32 v156, v76, v77, s36 op_sel:[0,0,0,1]
	v_cvt_scalef32_pk_fp8_f32 v157, v80, v81, s36 op_sel:[0,0,0,1]
	v_exp_f32_e32 v98, v98
	v_exp_f32_e32 v99, v99
	v_mfma_f32_32x32x64_f8f6f4 v[34:49], v[146:153], v[138:145], v[34:49]
	v_exp_f32_e32 v100, v100
	v_exp_f32_e32 v101, v101
	v_exp_f32_e32 v102, v102
	v_exp_f32_e32 v103, v103
	v_exp_f32_e32 v104, v104
	v_exp_f32_e32 v105, v105
	v_exp_f32_e32 v106, v106
	v_exp_f32_e32 v107, v107
	v_exp_f32_e32 v108, v108
	v_exp_f32_e32 v109, v109
	v_exp_f32_e32 v110, v110
	v_exp_f32_e32 v111, v111
	v_exp_f32_e32 v112, v112
	v_exp_f32_e32 v113, v113
	ds_read_b128 v[194:197], v234
	ds_read_b128 v[198:201], v234 offset:16
	v_pk_add_f32 v[66:67], v[232:233], v[98:99]
	v_pk_add_f32 v[68:69], v[230:231], v[100:101]
	v_pk_add_f32 v[66:67], v[102:103], v[66:67]
	v_pk_add_f32 v[68:69], v[104:105], v[68:69]
	v_pk_add_f32 v[66:67], v[106:107], v[66:67]
	v_pk_add_f32 v[68:69], v[108:109], v[68:69]
	v_pk_add_f32 v[140:141], v[110:111], v[66:67]
	v_pk_add_f32 v[138:139], v[112:113], v[68:69]
	v_mfma_f32_32x32x64_f8f6f4 v[18:33], v[146:153], v[130:137], v[18:33]
	v_exp_f32_e32 v82, v82
	v_exp_f32_e32 v83, v83
	v_exp_f32_e32 v84, v84
	v_exp_f32_e32 v85, v85
	v_exp_f32_e32 v86, v86
	v_exp_f32_e32 v87, v87
	v_exp_f32_e32 v88, v88
	v_exp_f32_e32 v89, v89
	v_exp_f32_e32 v90, v90
	v_exp_f32_e32 v91, v91
	v_exp_f32_e32 v92, v92
	v_exp_f32_e32 v93, v93
	v_exp_f32_e32 v94, v94
	v_exp_f32_e32 v95, v95
	v_exp_f32_e32 v96, v96
	v_exp_f32_e32 v97, v97
	v_pk_add_f32 v[66:67], v[192:193], v[82:83]
	v_pk_add_f32 v[68:69], v[190:191], v[84:85]
	v_pk_add_f32 v[66:67], v[86:87], v[66:67]
	v_pk_add_f32 v[68:69], v[88:89], v[68:69]
	v_pk_add_f32 v[130:131], v[90:91], v[66:67]
	v_pk_add_f32 v[132:133], v[92:93], v[68:69]
	s_waitcnt lgkmcnt(0)
; DI void attn_unit_d8(unsigned char* lds, const AttnArgs& a) {
;     ...
;     auto expsum = [&](f32x16& sc, f32x4& l) __attribute__((always_inline)) {
; #pragma unroll
;         for (int i = 0; i < 16; ++i) sc[i] = __builtin_amdgcn_exp2f(sc[i]);
; #pragma unroll
;         for (int i = 0; i < 4; ++i) l += (f32x4){sc[4 * i], sc[4 * i + 1], sc[4 * i + 2], sc[4 * i + 3]};
;     };
;     auto pack8 = [&](const f32x16& s0, const f32x16& s1) __attribute__((always_inline)) -> v8i { v8i p;
; #pragma unroll
;         for (int g = 0; g < 4; ++g) { p[g] = (int)pk4_fp8_div16(s0[4 * g], s0[4 * g + 1], s0[4 * g + 2], s0[4 * g + 3]); p[4 + g] = (int)pk4_fp8_div16(s1[4 * g], s1[4 * g + 1], s1[4 * g + 2], s1[4 * g + 3]); }
;         return p; };
;     auto pack4 = [&](const f32x16& sc, v8i& p, const int o) __attribute__((always_inline)) {
; #pragma unroll
;         for (int g = 0; g < 4; ++g) p[o + g] = (int)pk4_fp8_div16(sc[4 * g], sc[4 * g + 1], sc[4 * g + 2], sc[4 * g + 3]); };
;     auto qk = [&](const unsigned char* Kb, int hh, f32x16& sa, f32x16& sb) __attribute__((always_inline)) { const v8i kf = rd32(Kb + koff + hh * 32 * A8_PITCH);
;         sa = mfma8(kf, qfa, (f32x16){}); sb = mfma8(kf, qfb, (f32x16){}); };
;     gload(a.t0, kreg0, vreg0); gload(a.t0 + 1, kreg1, vreg1); lstore(0, kreg0, vreg0); lstore(1, kreg1, vreg1);
;     gload(a.t0 + 2, kreg0, vreg0); lstore(2, kreg0, vreg0);
;     __syncthreads();
;     asm volatile("" : "+v"(qfa), "+v"(qfb));
;     f32x16 s0a, s0b, s1a, s1b;
;     qk(lds, 0, s0a, s0b);
;     if (wid >= 4) __builtin_amdgcn_s_setprio(1);
;     int sb = 0;
;     const v8i zz8 = (v8i){0, 0, 0, 0, 0, 0, 0, 0};
;     v8i PaX = zz8, PbX = zz8, PaY = zz8, PbY = zz8, vX0 = zz8, vX1 = zz8, vY0 = zz8, vY1 = zz8;
;     auto tile = [&](const unsigned char* Kb, const unsigned char* Kn, v8i& Pa, v8i& Pb, v8i& v0, v8i& v1, const v8i& Qa, const v8i& Qb, const v8i& w0, const v8i& w1) __attribute__((always_inline)) {
;         qk(Kb, 1, s1a, s1b);
;         v0 = rd32(Kb + voff); v1 = rd32(Kb + voff + 32 * A8_PITCH);
;         o0[0] = mfma8(w0, Qa, o0[0]); o1[0] = mfma8(w0, Qb, o1[0]); o0[1] = mfma8(w1, Qa, o0[1]); o1[1] = mfma8(w1, Qb, o1[1]);
;         expsum(s0a, l0); expsum(s0b, l1); pack4(s0a, Pa, 0); pack4(s0b, Pb, 0);
;         qk(Kn, 0, s0a, s0b);
;         expsum(s1a, l0); expsum(s1b, l1); pack4(s1a, Pa, 4); pack4(s1b, Pb, 4);
; #pragma unroll
	v_mfma_f32_32x32x64_f8f6f4 v[66:81], v[194:201], v[114:121], 0
	v_cvt_scalef32_pk_fp8_f32 v190, v98, v99, s36
	v_cvt_scalef32_pk_fp8_f32 v191, v102, v103, s36
	v_cvt_scalef32_pk_fp8_f32 v192, v106, v107, s36
	v_cvt_scalef32_pk_fp8_f32 v193, v110, v111, s36
	v_cvt_scalef32_pk_fp8_f32 v158, v82, v83, s36
	v_cvt_scalef32_pk_fp8_f32 v159, v86, v87, s36
	v_pk_add_f32 v[142:143], v[96:97], v[132:133]
	v_pk_add_f32 v[144:145], v[94:95], v[130:131]
	v_cvt_scalef32_pk_fp8_f32 v160, v90, v91, s36
	v_cvt_scalef32_pk_fp8_f32 v190, v100, v101, s36 op_sel:[0,0,0,1]
	v_cvt_scalef32_pk_fp8_f32 v191, v104, v105, s36 op_sel:[0,0,0,1]
	v_cvt_scalef32_pk_fp8_f32 v192, v108, v109, s36 op_sel:[0,0,0,1]
	v_cvt_scalef32_pk_fp8_f32 v193, v112, v113, s36 op_sel:[0,0,0,1]
	v_cvt_scalef32_pk_fp8_f32 v158, v84, v85, s36 op_sel:[0,0,0,1]
	v_cvt_scalef32_pk_fp8_f32 v159, v88, v89, s36 op_sel:[0,0,0,1]
	v_mfma_f32_32x32x64_f8f6f4 v[98:113], v[194:201], v[122:129], 0
	global_load_dwordx2 v[194:195], v[220:221], off
	global_load_dwordx2 v[196:197], v[222:223], off
	ds_read_b128 v[130:133], v234 offset:2560
	ds_read_b128 v[134:137], v234 offset:2576
	v_exp_f32_e32 v146, v66
	s_add_i32 s80, s61, 0
	v_exp_f32_e32 v147, v67
	s_lshr_b32 s73, s80, 2
	s_mulk_i32 s52, 0x2800
	s_add_i32 s8, s52, 0
	v_cvt_scalef32_pk_fp8_f32 v161, v94, v95, s36
	v_add_u32_e32 v224, s8, v183
	v_cvt_scalef32_pk_fp8_f32 v160, v92, v93, s36 op_sel:[0,0,0,1]
	v_cvt_scalef32_pk_fp8_f32 v161, v96, v97, s36 op_sel:[0,0,0,1]
	v_exp_f32_e32 v148, v68
	s_lshl_b32 s73, s73, 9
	v_exp_f32_e32 v149, v69
	s_add_i32 s73, s73, s46
	v_exp_f32_e32 v150, v70
	s_mul_i32 s75, s73, 0xaaab
	v_exp_f32_e32 v151, v71
	s_lshr_b32 s75, s75, 22
	v_exp_f32_e32 v152, v72
	s_mul_i32 s76, s75, 0x60
	v_exp_f32_e32 v153, v73
	s_sub_i32 s76, s73, s76
	v_exp_f32_e32 v198, v74
	s_lshr_b32 s77, s76, 6
	v_exp_f32_e32 v199, v75
	s_lshl_b32 s78, s77, 6
	v_exp_f32_e32 v200, v76
	s_sub_i32 s76, s76, s78
	v_exp_f32_e32 v201, v77
	s_sub_i32 s78, 3, s77
	v_exp_f32_e32 v202, v78
	s_lshr_b32 s79, s76, s78
	v_exp_f32_e32 v203, v79
	s_lshl_b32 s79, s79, 2
	v_exp_f32_e32 v220, v80
	s_and_b32 s81, s80, 3
	v_exp_f32_e32 v221, v81
	s_add_i32 s79, s79, s81
	v_pk_add_f32 v[66:67], v[140:141], v[146:147]
	s_waitcnt lgkmcnt(0)
; DI void attn_unit_d8(unsigned char* lds, const AttnArgs& a) {
;     ...
;     auto expsum = [&](f32x16& sc, f32x4& l) __attribute__((always_inline)) {
; #pragma unroll
;         for (int i = 0; i < 16; ++i) sc[i] = __builtin_amdgcn_exp2f(sc[i]);
; #pragma unroll
;         for (int i = 0; i < 4; ++i) l += (f32x4){sc[4 * i], sc[4 * i + 1], sc[4 * i + 2], sc[4 * i + 3]};
;     };
;     auto pack8 = [&](const f32x16& s0, const f32x16& s1) __attribute__((always_inline)) -> v8i { v8i p;
; #pragma unroll
;         for (int g = 0; g < 4; ++g) { p[g] = (int)pk4_fp8_div16(s0[4 * g], s0[4 * g + 1], s0[4 * g + 2], s0[4 * g + 3]); p[4 + g] = (int)pk4_fp8_div16(s1[4 * g], s1[4 * g + 1], s1[4 * g + 2], s1[4 * g + 3]); }
;         return p; };
;     auto pack4 = [&](const f32x16& sc, v8i& p, const int o) __attribute__((always_inline)) {
; #pragma unroll
;         for (int g = 0; g < 4; ++g) p[o + g] = (int)pk4_fp8_div16(sc[4 * g], sc[4 * g + 1], sc[4 * g + 2], sc[4 * g + 3]); };
;     auto qk = [&](const unsigned char* Kb, int hh, f32x16& sa, f32x16& sb) __attribute__((always_inline)) { const v8i kf = rd32(Kb + koff + hh * 32 * A8_PITCH);
;         sa = mfma8(kf, qfa, (f32x16){}); sb = mfma8(kf, qfb, (f32x16){}); };
;     gload(a.t0, kreg0, vreg0); gload(a.t0 + 1, kreg1, vreg1); lstore(0, kreg0, vreg0); lstore(1, kreg1, vreg1);
;     gload(a.t0 + 2, kreg0, vreg0); lstore(2, kreg0, vreg0);
;     __syncthreads();
;     asm volatile("" : "+v"(qfa), "+v"(qfb));
;     f32x16 s0a, s0b, s1a, s1b;
;     qk(lds, 0, s0a, s0b);
;     if (wid >= 4) __builtin_amdgcn_s_setprio(1);
;     int sb = 0;
;     const v8i zz8 = (v8i){0, 0, 0, 0, 0, 0, 0, 0};
;     v8i PaX = zz8, PbX = zz8, PaY = zz8, PbY = zz8, vX0 = zz8, vX1 = zz8, vY0 = zz8, vY1 = zz8;
;     auto tile = [&](const unsigned char* Kb, const unsigned char* Kn, v8i& Pa, v8i& Pb, v8i& v0, v8i& v1, const v8i& Qa, const v8i& Qb, const v8i& w0, const v8i& w1) __attribute__((always_inline)) {
;         qk(Kb, 1, s1a, s1b);
;         v0 = rd32(Kb + voff); v1 = rd32(Kb + voff + 32 * A8_PITCH);
;         o0[0] = mfma8(w0, Qa, o0[0]); o1[0] = mfma8(w0, Qb, o1[0]); o0[1] = mfma8(w1, Qa, o0[1]); o1[1] = mfma8(w1, Qb, o1[1]);
;         expsum(s0a, l0); expsum(s0b, l1); pack4(s0a, Pa, 0); pack4(s0b, Pb, 0);
;         qk(Kn, 0, s0a, s0b);
;         expsum(s1a, l0); expsum(s1b, l1); pack4(s1a, Pa, 4); pack4(s1b, Pb, 4);
; #pragma unroll
	v_mfma_f32_32x32x64_f8f6f4 v[82:97], v[130:137], v[114:121], 0
	v_pk_add_f32 v[68:69], v[138:139], v[148:149]
	v_pk_add_f32 v[66:67], v[150:151], v[66:67]
	v_pk_add_f32 v[68:69], v[152:153], v[68:69]
	v_pk_add_f32 v[138:139], v[198:199], v[66:67]
	v_pk_add_f32 v[140:141], v[200:201], v[68:69]
	v_exp_f32_e32 v98, v98
	s_lshl_b32 s79, s79, 5
	v_exp_f32_e32 v99, v99
	s_lshl_b32 s81, s63, 2
	v_exp_f32_e32 v100, v100
	s_add_i32 s81, s81, s79
	v_exp_f32_e32 v101, v101
	s_sub_i32 s78, 13, s77
	v_exp_f32_e32 v102, v102
	s_lshl_b32 s81, s81, s78
	v_exp_f32_e32 v103, v103
	s_lshr_b32 s78, 7, s77
	v_exp_f32_e32 v104, v104
	s_and_b32 s78, s76, s78
	v_exp_f32_e32 v105, v105
	s_lshl_b32 s72, s78, 10
	v_exp_f32_e32 v106, v106
	s_add_i32 s81, s81, s72
	v_exp_f32_e32 v107, v107
	s_add_i32 s72, s75, 32
	v_exp_f32_e32 v108, v108
	s_sub_i32 s80, 23, s77
	v_exp_f32_e32 v109, v109
	s_lshl_b32 s72, s72, s80
	v_exp_f32_e32 v110, v110
	s_add_i32 s81, s81, s72
	v_exp_f32_e32 v111, v111
	s_cmp_eq_u32 s77, 0
	s_cselect_b64 s[84:85], s[66:67], s[68:69]
	v_exp_f32_e32 v112, v112
	s_add_u32 s84, s84, s81
	s_addc_u32 s85, s85, 0
	v_exp_f32_e32 v113, v113
	s_lshr_b32 s80, 0x2000, s77
	v_exp_f32_e32 v82, v82
	s_and_b32 s72, s78, 3
	v_mfma_f32_32x32x64_f8f6f4 v[66:81], v[130:137], v[122:129], 0
	v_pk_add_f32 v[130:131], v[144:145], v[98:99]
	v_pk_add_f32 v[132:133], v[142:143], v[100:101]
	v_pk_add_f32 v[142:143], v[102:103], v[130:131]
	v_pk_add_f32 v[132:133], v[104:105], v[132:133]
	v_pk_add_f32 v[134:135], v[220:221], v[140:141]
	v_pk_add_f32 v[136:137], v[202:203], v[138:139]
	v_pk_add_f32 v[142:143], v[106:107], v[142:143]
	v_pk_add_f32 v[132:133], v[108:109], v[132:133]
	v_cvt_scalef32_pk_fp8_f32 v138, v146, v147, s36
	v_cvt_scalef32_pk_fp8_f32 v139, v150, v151, s36
	v_cvt_scalef32_pk_fp8_f32 v140, v198, v199, s36
	v_cvt_scalef32_pk_fp8_f32 v141, v202, v203, s36
	v_cvt_scalef32_pk_fp8_f32 v130, v98, v99, s36
	v_cvt_scalef32_pk_fp8_f32 v131, v102, v103, s36
	v_pk_add_f32 v[146:147], v[112:113], v[132:133]
	v_pk_add_f32 v[150:151], v[110:111], v[142:143]
	v_mfma_f32_32x32x64_f8f6f4 v[50:65], v[170:177], v[186:193], v[50:65]
	v_exp_f32_e32 v83, v83
	s_lshl_b32 s72, s72, 19
	v_exp_f32_e32 v84, v84
	s_lshr_b32 s81, s78, 2
	v_exp_f32_e32 v85, v85
	s_lshl_b32 s81, s81, 17
	v_add_u32_e32 v102, s50, v219
	v_exp_f32_e32 v86, v86
	s_add_i32 s72, s72, s81
	v_exp_f32_e32 v87, v87
	s_lshl_b32 s81, s78, 18
	v_exp_f32_e32 v88, v88
	s_cmp_eq_u32 s77, 0
	s_cselect_b32 s72, s72, s81
	v_exp_f32_e32 v89, v89
	s_mul_i32 s81, s77, 0xc000000
	v_cvt_scalef32_pk_fp8_f32 v130, v100, v101, s36 op_sel:[0,0,0,1]
	v_cvt_scalef32_pk_fp8_f32 v131, v104, v105, s36 op_sel:[0,0,0,1]
	v_exp_f32_e32 v90, v90
	s_add_i32 s81, s81, 0x9094000
	v_exp_f32_e32 v91, v91
	s_add_i32 s72, s72, s79
	v_exp_f32_e32 v92, v92
	s_sub_i32 s73, 21, s77
	v_exp_f32_e32 v93, v93
	s_lshl_b32 s73, s75, s73
	ds_read_b128 v[98:101], v102
	ds_read_b128 v[102:105], v102 offset:16
	v_cvt_scalef32_pk_fp8_f32 v138, v148, v149, s36 op_sel:[0,0,0,1]
	v_cvt_scalef32_pk_fp8_f32 v139, v152, v153, s36 op_sel:[0,0,0,1]
	v_cvt_scalef32_pk_fp8_f32 v140, v200, v201, s36 op_sel:[0,0,0,1]
	v_cvt_scalef32_pk_fp8_f32 v141, v220, v221, s36 op_sel:[0,0,0,1]
	v_exp_f32_e32 v94, v94
	s_add_i32 s72, s72, s73
	v_exp_f32_e32 v95, v95
	s_add_u32 s72, s72, s81
	v_mfma_f32_32x32x64_f8f6f4 v[2:17], v[170:177], v[154:161], v[2:17]
	v_exp_f32_e32 v148, v96
	s_or_b32 s79, s72, s77
	v_cvt_scalef32_pk_fp8_f32 v132, v106, v107, s36
	v_exp_f32_e32 v149, v97
	v_pk_add_f32 v[96:97], v[136:137], v[82:83]
	v_pk_add_f32 v[106:107], v[134:135], v[84:85]
	v_exp_f32_e32 v66, v66
	v_exp_f32_e32 v67, v67
	v_exp_f32_e32 v68, v68
	v_exp_f32_e32 v69, v69
	v_cvt_scalef32_pk_fp8_f32 v133, v110, v111, s36
	v_pk_add_f32 v[106:107], v[88:89], v[106:107]
	v_pk_add_f32 v[96:97], v[86:87], v[96:97]
	v_exp_f32_e32 v70, v70
	v_exp_f32_e32 v71, v71
	v_exp_f32_e32 v72, v72
	v_exp_f32_e32 v73, v73
	v_cvt_scalef32_pk_fp8_f32 v132, v108, v109, s36 op_sel:[0,0,0,1]
	v_cvt_scalef32_pk_fp8_f32 v133, v112, v113, s36 op_sel:[0,0,0,1]
	v_pk_add_f32 v[96:97], v[90:91], v[96:97]
	v_pk_add_f32 v[106:107], v[92:93], v[106:107]
	v_exp_f32_e32 v74, v74
	v_exp_f32_e32 v75, v75
	v_mfma_f32_32x32x64_f8f6f4 v[34:49], v[162:169], v[186:193], v[34:49]
	v_exp_f32_e32 v76, v76
	v_exp_f32_e32 v77, v77
	v_exp_f32_e32 v78, v78
	v_exp_f32_e32 v79, v79
	v_exp_f32_e32 v80, v80
	v_exp_f32_e32 v81, v81
	v_cvt_scalef32_pk_fp8_f32 v142, v82, v83, s36
	v_cvt_scalef32_pk_fp8_f32 v143, v86, v87, s36
	v_cvt_scalef32_pk_fp8_f32 v144, v90, v91, s36
	v_cvt_scalef32_pk_fp8_f32 v142, v84, v85, s36 op_sel:[0,0,0,1]
	v_pk_add_f32 v[82:83], v[150:151], v[66:67]
	v_pk_add_f32 v[84:85], v[146:147], v[68:69]
	s_mulk_i32 s53, 0x2800
	v_pk_add_f32 v[186:187], v[148:149], v[106:107]
	v_pk_add_f32 v[188:189], v[94:95], v[96:97]
	v_cvt_scalef32_pk_fp8_f32 v145, v94, v95, s36
	v_cvt_scalef32_pk_fp8_f32 v143, v88, v89, s36 op_sel:[0,0,0,1]
	v_cvt_scalef32_pk_fp8_f32 v144, v92, v93, s36 op_sel:[0,0,0,1]
	v_pk_add_f32 v[84:85], v[72:73], v[84:85]
	v_mfma_f32_32x32x64_f8f6f4 v[18:33], v[162:169], v[154:161], v[18:33]
	v_pk_add_f32 v[82:83], v[70:71], v[82:83]
	s_add_i32 s51, s53, 0
	v_pk_add_f32 v[82:83], v[74:75], v[82:83]
	v_pk_add_f32 v[84:85], v[76:77], v[84:85]
	v_cvt_scalef32_pk_fp8_f32 v134, v66, v67, s36
	v_cvt_scalef32_pk_fp8_f32 v135, v70, v71, s36
	v_cvt_scalef32_pk_fp8_f32 v136, v74, v75, s36
	v_cvt_scalef32_pk_fp8_f32 v137, v78, v79, s36
	v_pk_add_f32 v[190:191], v[80:81], v[84:85]
	v_pk_add_f32 v[192:193], v[78:79], v[82:83]
	v_add_u32_e32 v106, s8, v218
	v_add_u32_e32 v107, s51, v183
	v_cvt_scalef32_pk_fp8_f32 v145, v148, v149, s36 op_sel:[0,0,0,1]
	v_cvt_scalef32_pk_fp8_f32 v134, v68, v69, s36 op_sel:[0,0,0,1]
	v_cvt_scalef32_pk_fp8_f32 v135, v72, v73, s36 op_sel:[0,0,0,1]
	v_cvt_scalef32_pk_fp8_f32 v136, v76, v77, s36 op_sel:[0,0,0,1]
	v_cvt_scalef32_pk_fp8_f32 v137, v80, v81, s36 op_sel:[0,0,0,1]
	s_waitcnt lgkmcnt(0)
	v_mfma_f32_32x32x64_f8f6f4 v[82:97], v[98:105], v[114:121], 0
	ds_read_b128 v[154:157], v234 offset:5120
	ds_read_b128 v[158:161], v234 offset:5136
	ds_read_b128 v[146:149], v234 offset:7680
	ds_read_b128 v[150:153], v234 offset:7696
	s_cmpk_gt_i32 s46, 0x1ff
	s_cbranch_scc1 .Lmy_rd1_ldum
	s_add_i32 s72, s61, -1
	s_cmp_lt_u32 s72, 24
	s_cbranch_scc0 .Lmy_rd1_noc
	s_waitcnt vmcnt(4)
	v_cvt_scalef32_pk_fp8_f32 v236, v236, v240, s62
	v_cvt_scalef32_pk_fp8_f32 v237, v237, v241, s62
	v_cvt_scalef32_pk_fp8_f32 v238, v238, v242, s62
	v_cvt_scalef32_pk_fp8_f32 v239, v239, v243, s62
	v_cvt_scalef32_pk_fp8_f32 v236, v244, v248, s62 op_sel:[0,0,0,1]
	v_cvt_scalef32_pk_fp8_f32 v237, v245, v249, s62 op_sel:[0,0,0,1]
	v_cvt_scalef32_pk_fp8_f32 v238, v246, v250, s62 op_sel:[0,0,0,1]
	v_cvt_scalef32_pk_fp8_f32 v239, v247, v251, s62 op_sel:[0,0,0,1]
	ds_write_b32 v252, v236
	ds_write_b32 v252, v237 offset:36
	ds_write_b32 v252, v238 offset:72
	ds_write_b32 v252, v239 offset:108

; DI void attn_unit_a8(unsigned char* lds, const AttnArgs& a) {
;     ...
;     auto expsum = [&](f32x16& sc) __attribute__((always_inline)) {
; #pragma unroll
;         for (int i = 0; i < 16; ++i) sc[i] = __builtin_amdgcn_exp2f(sc[i]);
; #pragma unroll
;         for (int i = 0; i < 4; ++i) l0 += (f32x4){sc[4 * i], sc[4 * i + 1], sc[4 * i + 2], sc[4 * i + 3]};
;     };
;     auto pack8 = [&](const f32x16& s0, const f32x16& s1) __attribute__((always_inline)) -> v8i { v8i p;
; #pragma unroll
;         for (int g = 0; g < 4; ++g) { p[g] = (int)pk4_fp8_div16(s0[4 * g], s0[4 * g + 1], s0[4 * g + 2], s0[4 * g + 3]); p[4 + g] = (int)pk4_fp8_div16(s1[4 * g], s1[4 * g + 1], s1[4 * g + 2], s1[4 * g + 3]); }
;         return p; };
;     f32x4 wq[4];
;     const int wn4 = (tid & 63) * 4;
;     constexpr int WPITCH = 36;
;     auto w_decode = [&](int j, const float*& src, unsigned char*& dst, int& ld, int& n0, int& k0, bool& gu) __attribute__((always_inline)) {
;         const int g = (j >> 2) * 512 + a.wl, e = g / 96, rr = g - e * 96; KParamsPtr kp = kparams();
;         if (rr < 64) { src = kp->w_gu + ((size_t)a.wli * NE + e) * (1024 * 2048); dst = kp->ws + WS_WGU + (size_t)a.wli * SZ_WGU + (size_t)e * 2048 * 1024; ld = 2048; n0 = (rr & 7) * 256; k0 = ((rr >> 3) * 4 + (j & 3)) * 32; gu = true; }
;         else { const int q = rr - 64; src = kp->w_dn + ((size_t)a.wli * NE + e) * (1024 * 1024); dst = kp->ws + WS_WDN + (size_t)a.wli * SZ_WDN + (size_t)e * 1024 * 1024; ld = 1024; n0 = (q & 3) * 256; k0 = ((q >> 2) * 4 + (j & 3)) * 32; gu = false; } };
;     auto w_issue = [&](int j) __attribute__((always_inline)) { const float* src; unsigned char* dst; int ld, n0, k0; bool gu; w_decode(j, src, dst, ld, n0, k0, gu);
;         const float* p = src + (size_t)(k0 + 4 * wid) * ld + n0 + wn4;
;         wq[0] = __builtin_nontemporal_load((const f32x4*)p); wq[1] = __builtin_nontemporal_load((const f32x4*)(p + ld));
;         wq[2] = __builtin_nontemporal_load((const f32x4*)(p + (size_t)2 * ld)); wq[3] = __builtin_nontemporal_load((const f32x4*)(p + (size_t)3 * ld)); };
;     auto w_cvt = [&]() __attribute__((always_inline)) { unsigned char* t8 = lds + AT_WT + wn4 * WPITCH + 4 * wid;
; #pragma unroll
;         for (int j = 0; j < 4; ++j) *(unsigned*)(t8 + j * WPITCH) = pk4_fp8_mul64(wq[0][j], wq[1][j], wq[2][j], wq[3][j]); };
;     const int wcol = tid >> 1, whalf = tid & 1;
.LBB0_1934:
	s_min_u32 s8, s50, 64
	s_cmp_lt_u32 s50, 61
	s_cselect_b64 s[10:11], -1, 0
	s_lshl_b32 s8, s8, 6
	s_add_i32 s15, s8, 0xc0
	s_add_i32 s18, s8, 0xfffff0c0
	s_and_b64 s[16:17], s[10:11], exec
	s_cselect_b32 s15, s15, s18
	s_mov_b32 s18, s14
	s_add_i32 s14, s14, 1
	s_cmp_lg_u32 s18, 2
	s_cselect_b32 s14, s14, 0
	s_mul_i32 s19, s14, 0x4680
	v_add_u32_e32 v106, s19, v169
	ds_read_b128 v[50:53], v106
	ds_read_b128 v[54:57], v106 offset:16
	v_add_u32_e32 v58, s15, v130
	s_and_b64 s[10:11], s[10:11], exec
	v_ashrrev_i32_e32 v59, 31, v58
	s_cselect_b32 s16, s42, s12
	s_cselect_b32 s17, s43, s13
	s_waitcnt lgkmcnt(0)
	v_mfma_f32_32x32x64_f8f6f4 v[34:49], v[50:57], v[98:105], 0
	v_lshlrev_b64 v[50:51], 7, v[58:59]
	v_lshl_add_u64 v[50:51], s[16:17], 0, v[50:51]
	v_lshl_add_u64 v[50:51], v[50:51], 0, v[132:133]
	v_lshl_add_u64 v[58:59], v[134:135], 0, s[8:9]
	global_load_dwordx2 v[112:113], v[50:51], off
	ds_read_b128 v[50:53], v106 offset:2560
	ds_read_b128 v[54:57], v106 offset:2576
	global_load_dwordx2 v[114:115], v[58:59], off offset:192
	s_mulk_i32 s18, 0x4680
	v_add_u32_e32 v58, s18, v169
	v_exp_f32_e32 v82, v82
	v_exp_f32_e32 v83, v83
	v_exp_f32_e32 v86, v86
	v_exp_f32_e32 v87, v87
	v_exp_f32_e32 v90, v90
	v_exp_f32_e32 v91, v91
	v_exp_f32_e32 v94, v94
	v_exp_f32_e32 v95, v95
	v_exp_f32_e32 v124, v66
	v_exp_f32_e32 v125, v67
	v_exp_f32_e32 v148, v70
	v_exp_f32_e32 v149, v71
	v_exp_f32_e32 v74, v74
	v_exp_f32_e32 v75, v75
	v_exp_f32_e32 v78, v78
	v_exp_f32_e32 v79, v79
	ds_read_b128 v[116:119], v58 offset:5120
	ds_read_b128 v[120:123], v58 offset:5136
	ds_read_b128 v[140:143], v58 offset:7680
	ds_read_b128 v[144:147], v58 offset:7696
	v_exp_f32_e32 v84, v84
	v_exp_f32_e32 v85, v85
	v_exp_f32_e32 v88, v88
	v_exp_f32_e32 v89, v89
	v_exp_f32_e32 v92, v92
	v_exp_f32_e32 v93, v93
	v_exp_f32_e32 v96, v96
	v_exp_f32_e32 v97, v97
	v_exp_f32_e32 v126, v68
	v_exp_f32_e32 v127, v69
	v_exp_f32_e32 v150, v72
	v_exp_f32_e32 v151, v73
	v_exp_f32_e32 v76, v76
	v_exp_f32_e32 v77, v77
	v_exp_f32_e32 v80, v80
	v_exp_f32_e32 v81, v81
	v_cvt_scalef32_pk_fp8_f32 v66, v82, v83, s69
	v_cvt_scalef32_pk_fp8_f32 v70, v124, v125, s69
	v_cvt_scalef32_pk_fp8_f32 v67, v86, v87, s69
	v_cvt_scalef32_pk_fp8_f32 v71, v148, v149, s69
	v_cvt_scalef32_pk_fp8_f32 v68, v90, v91, s69
	v_cvt_scalef32_pk_fp8_f32 v72, v74, v75, s69
	v_cvt_scalef32_pk_fp8_f32 v69, v94, v95, s69
	v_cvt_scalef32_pk_fp8_f32 v73, v78, v79, s69
	v_cvt_scalef32_pk_fp8_f32 v66, v84, v85, s69 op_sel:[0,0,0,1]
	v_cvt_scalef32_pk_fp8_f32 v70, v126, v127, s69 op_sel:[0,0,0,1]
	v_cvt_scalef32_pk_fp8_f32 v67, v88, v89, s69 op_sel:[0,0,0,1]
	v_cvt_scalef32_pk_fp8_f32 v71, v150, v151, s69 op_sel:[0,0,0,1]
	v_cvt_scalef32_pk_fp8_f32 v68, v92, v93, s69 op_sel:[0,0,0,1]
	v_cvt_scalef32_pk_fp8_f32 v72, v76, v77, s69 op_sel:[0,0,0,1]
	v_cvt_scalef32_pk_fp8_f32 v69, v96, v97, s69 op_sel:[0,0,0,1]
	v_cvt_scalef32_pk_fp8_f32 v73, v80, v81, s69 op_sel:[0,0,0,1]
	s_waitcnt lgkmcnt(4)
	v_mfma_f32_32x32x64_f8f6f4 v[50:65], v[50:57], v[98:105], 0
	s_add_i32 s15, s19, 0x4680
	s_cmp_eq_u32 s14, 2
	v_pk_add_f32 v[110:111], v[110:111], v[84:85]
	v_pk_add_f32 v[82:83], v[108:109], v[82:83]
	s_cselect_b64 s[10:11], -1, 0
	v_pk_add_f32 v[84:85], v[88:89], v[110:111]
	v_pk_add_f32 v[82:83], v[86:87], v[82:83]
	v_pk_add_f32 v[84:85], v[92:93], v[84:85]
	v_pk_add_f32 v[82:83], v[90:91], v[82:83]
	s_and_b64 s[16:17], s[10:11], exec
	v_pk_add_f32 v[84:85], v[96:97], v[84:85]
	v_pk_add_f32 v[82:83], v[94:95], v[82:83]
	s_cselect_b32 s8, 0, s15
	v_pk_add_f32 v[82:83], v[124:125], v[82:83]
	v_pk_add_f32 v[84:85], v[126:127], v[84:85]
	s_waitcnt lgkmcnt(2)
	v_mfma_f32_32x32x64_f8f6f4 v[18:33], v[116:123], v[66:73], v[18:33]
	s_add_i32 s8, s8, 0
	v_pk_add_f32 v[84:85], v[150:151], v[84:85]
	v_pk_add_f32 v[82:83], v[148:149], v[82:83]
	v_pk_add_f32 v[76:77], v[76:77], v[84:85]
	v_pk_add_f32 v[74:75], v[74:75], v[82:83]
	v_pk_add_f32 v[110:111], v[80:81], v[76:77]
	v_pk_add_f32 v[108:109], v[78:79], v[74:75]
	s_cmpk_gt_u32 s50, 0x42
	s_waitcnt lgkmcnt(0)
	v_mfma_f32_32x32x64_f8f6f4 v[2:17], v[140:147], v[66:73], v[2:17]
	v_add_u32_e32 v66, s8, v131
	s_waitcnt vmcnt(3)
	ds_write_b64 v66, v[136:137]
	v_add_u32_e32 v66, s8, v168
	v_add_u32_e32 v66, 0x1400, v66
	s_waitcnt vmcnt(2)
	ds_write2_b32 v66, v138, v139 offset1:8
	s_waitcnt lgkmcnt(0)
	s_barrier
; DI void attn_unit_a8(unsigned char* lds, const AttnArgs& a) {
;     ...
;     auto expsum = [&](f32x16& sc) __attribute__((always_inline)) {
; #pragma unroll
;         for (int i = 0; i < 16; ++i) sc[i] = __builtin_amdgcn_exp2f(sc[i]);
; #pragma unroll
;         for (int i = 0; i < 4; ++i) l0 += (f32x4){sc[4 * i], sc[4 * i + 1], sc[4 * i + 2], sc[4 * i + 3]};
;     };
;     auto pack8 = [&](const f32x16& s0, const f32x16& s1) __attribute__((always_inline)) -> v8i { v8i p;
; #pragma unroll
;         for (int g = 0; g < 4; ++g) { p[g] = (int)pk4_fp8_div16(s0[4 * g], s0[4 * g + 1], s0[4 * g + 2], s0[4 * g + 3]); p[4 + g] = (int)pk4_fp8_div16(s1[4 * g], s1[4 * g + 1], s1[4 * g + 2], s1[4 * g + 3]); }
;         return p; };
;     f32x4 wq[4];
;     const int wn4 = (tid & 63) * 4;
;     constexpr int WPITCH = 36;
;     auto w_decode = [&](int j, const float*& src, unsigned char*& dst, int& ld, int& n0, int& k0, bool& gu) __attribute__((always_inline)) {
;         const int g = (j >> 2) * 512 + a.wl, e = g / 96, rr = g - e * 96; KParamsPtr kp = kparams();
;         if (rr < 64) { src = kp->w_gu + ((size_t)a.wli * NE + e) * (1024 * 2048); dst = kp->ws + WS_WGU + (size_t)a.wli * SZ_WGU + (size_t)e * 2048 * 1024; ld = 2048; n0 = (rr & 7) * 256; k0 = ((rr >> 3) * 4 + (j & 3)) * 32; gu = true; }
;         else { const int q = rr - 64; src = kp->w_dn + ((size_t)a.wli * NE + e) * (1024 * 1024); dst = kp->ws + WS_WDN + (size_t)a.wli * SZ_WDN + (size_t)e * 1024 * 1024; ld = 1024; n0 = (q & 3) * 256; k0 = ((q >> 2) * 4 + (j & 3)) * 32; gu = false; } };
;     auto w_issue = [&](int j) __attribute__((always_inline)) { const float* src; unsigned char* dst; int ld, n0, k0; bool gu; w_decode(j, src, dst, ld, n0, k0, gu);
;         const float* p = src + (size_t)(k0 + 4 * wid) * ld + n0 + wn4;
;         wq[0] = __builtin_nontemporal_load((const f32x4*)p); wq[1] = __builtin_nontemporal_load((const f32x4*)(p + ld));
;         wq[2] = __builtin_nontemporal_load((const f32x4*)(p + (size_t)2 * ld)); wq[3] = __builtin_nontemporal_load((const f32x4*)(p + (size_t)3 * ld)); };
;     auto w_cvt = [&]() __attribute__((always_inline)) { unsigned char* t8 = lds + AT_WT + wn4 * WPITCH + 4 * wid;
; #pragma unroll
;         for (int j = 0; j < 4; ++j) *(unsigned*)(t8 + j * WPITCH) = pk4_fp8_mul64(wq[0][j], wq[1][j], wq[2][j], wq[3][j]); };
;     const int wcol = tid >> 1, whalf = tid & 1;
	s_cbranch_scc1 .LBB0_1936
	s_min_u32 s8, s50, 63
	s_cmp_lt_u32 s50, 60
	s_cselect_b64 s[16:17], -1, 0
	s_lshl_b32 s8, s8, 6
	s_add_i32 s15, s8, 0x100
	s_add_i32 s20, s8, 0xfffff100
	s_and_b64 s[18:19], s[16:17], exec
	s_cselect_b32 s15, s15, s20
	s_add_i32 s14, s14, 1
	s_and_b64 s[10:11], s[10:11], exec
	v_add_u32_e32 v82, s15, v130
	s_cselect_b32 s14, 0, s14
	s_and_b64 s[16:17], s[16:17], exec
	v_ashrrev_i32_e32 v83, 31, v82
	s_cselect_b32 s17, s43, s13
	s_cselect_b32 s16, s42, s12
	v_lshlrev_b64 v[82:83], 7, v[82:83]
	s_mul_i32 s10, s14, 0x4680
	v_lshl_add_u64 v[90:91], s[16:17], 0, v[82:83]
	v_add_u32_e32 v86, s10, v169
	v_lshl_add_u64 v[90:91], v[90:91], 0, v[132:133]
	ds_read_b128 v[66:69], v86 offset:2560
	ds_read_b128 v[70:73], v86 offset:2576
	ds_read_b128 v[82:85], v86
	ds_read_b128 v[86:89], v86 offset:16
	global_load_dwordx2 v[136:137], v[90:91], off
	v_lshl_add_u64 v[90:91], v[134:135], 0, s[8:9]
	global_load_dwordx2 v[138:139], v[90:91], off offset:256
	v_exp_f32_e32 v124, v34
	v_exp_f32_e32 v125, v35
	v_exp_f32_e32 v36, v36
	v_exp_f32_e32 v37, v37
	v_exp_f32_e32 v126, v38
	v_exp_f32_e32 v127, v39
	v_exp_f32_e32 v42, v42
	v_exp_f32_e32 v43, v43
	v_exp_f32_e32 v46, v46
	v_exp_f32_e32 v47, v47
	v_exp_f32_e32 v50, v50
	v_exp_f32_e32 v51, v51
	v_exp_f32_e32 v54, v54
	v_exp_f32_e32 v55, v55
	v_exp_f32_e32 v58, v58
	v_exp_f32_e32 v59, v59
	v_exp_f32_e32 v62, v62
	v_exp_f32_e32 v63, v63
	ds_read_b128 v[116:119], v106 offset:5120
	ds_read_b128 v[120:123], v106 offset:5136
	ds_read_b128 v[140:143], v106 offset:7680
	ds_read_b128 v[144:147], v106 offset:7696
	v_exp_f32_e32 v148, v40
	v_exp_f32_e32 v149, v41
	v_exp_f32_e32 v44, v44
	v_exp_f32_e32 v45, v45
	v_exp_f32_e32 v48, v48
	v_exp_f32_e32 v49, v49
	v_exp_f32_e32 v52, v52
	v_exp_f32_e32 v53, v53
	v_exp_f32_e32 v56, v56
	v_exp_f32_e32 v57, v57
	v_exp_f32_e32 v60, v60
	v_exp_f32_e32 v61, v61
	v_exp_f32_e32 v64, v64
	v_exp_f32_e32 v65, v65
	v_cvt_scalef32_pk_fp8_f32 v34, v124, v125, s69
	v_pk_add_f32 v[110:111], v[110:111], v[36:37]
	v_cvt_scalef32_pk_fp8_f32 v34, v36, v37, s69 op_sel:[0,0,0,1]
	s_waitcnt lgkmcnt(6)
	v_mfma_f32_32x32x64_f8f6f4 v[66:81], v[66:73], v[98:105], 0
	v_cvt_scalef32_pk_fp8_f32 v38, v50, v51, s69
	v_cvt_scalef32_pk_fp8_f32 v35, v126, v127, s69
	v_cvt_scalef32_pk_fp8_f32 v39, v54, v55, s69
	v_cvt_scalef32_pk_fp8_f32 v36, v42, v43, s69
	v_cvt_scalef32_pk_fp8_f32 v40, v58, v59, s69
	v_cvt_scalef32_pk_fp8_f32 v37, v46, v47, s69
	v_cvt_scalef32_pk_fp8_f32 v41, v62, v63, s69
	v_cvt_scalef32_pk_fp8_f32 v38, v52, v53, s69 op_sel:[0,0,0,1]
	v_cvt_scalef32_pk_fp8_f32 v35, v148, v149, s69 op_sel:[0,0,0,1]
	v_cvt_scalef32_pk_fp8_f32 v39, v56, v57, s69 op_sel:[0,0,0,1]
	v_cvt_scalef32_pk_fp8_f32 v36, v44, v45, s69 op_sel:[0,0,0,1]
	v_cvt_scalef32_pk_fp8_f32 v40, v60, v61, s69 op_sel:[0,0,0,1]
	v_cvt_scalef32_pk_fp8_f32 v37, v48, v49, s69 op_sel:[0,0,0,1]
	v_cvt_scalef32_pk_fp8_f32 v41, v64, v65, s69 op_sel:[0,0,0,1]
	v_pk_add_f32 v[108:109], v[108:109], v[124:125]
	s_waitcnt lgkmcnt(4)
	v_mfma_f32_32x32x64_f8f6f4 v[82:97], v[82:89], v[98:105], 0
	s_addk_i32 s10, 0x4680
	v_pk_add_f32 v[110:111], v[148:149], v[110:111]
	v_pk_add_f32 v[108:109], v[126:127], v[108:109]
	s_cmp_lg_u32 s14, 2
	v_pk_add_f32 v[42:43], v[42:43], v[108:109]
	v_pk_add_f32 v[44:45], v[44:45], v[110:111]
	s_cselect_b32 s8, s10, 0
	v_pk_add_f32 v[44:45], v[48:49], v[44:45]
	v_pk_add_f32 v[42:43], v[46:47], v[42:43]
	s_add_i32 s8, s8, 0
	v_pk_add_f32 v[42:43], v[50:51], v[42:43]
	v_pk_add_f32 v[44:45], v[52:53], v[44:45]
	v_pk_add_f32 v[42:43], v[54:55], v[42:43]
	v_pk_add_f32 v[44:45], v[56:57], v[44:45]
	v_pk_add_f32 v[42:43], v[58:59], v[42:43]
	s_waitcnt lgkmcnt(2)
	v_mfma_f32_32x32x64_f8f6f4 v[18:33], v[116:123], v[34:41], v[18:33]
	v_pk_add_f32 v[44:45], v[60:61], v[44:45]
	v_pk_add_f32 v[108:109], v[62:63], v[42:43]
	v_pk_add_f32 v[110:111], v[64:65], v[44:45]
	s_waitcnt lgkmcnt(0)
	v_mfma_f32_32x32x64_f8f6f4 v[2:17], v[140:147], v[34:41], v[2:17]
	v_add_u32_e32 v34, s8, v131
	s_waitcnt vmcnt(3)
	ds_write_b64 v34, v[112:113]
	v_add_u32_e32 v34, s8, v168
	v_add_u32_e32 v34, 0x1400, v34
	s_waitcnt vmcnt(2)
	ds_write2_b32 v34, v114, v115 offset1:8
	s_waitcnt lgkmcnt(0)
	s_barrier
